# baseline (speedup 1.0000x reference)
_Z13expert_kernelPKfS0_PKcPf:
	s_load_dwordx2 s[20:21], s[0:1], 0x10
	s_load_dwordx2 s[22:23], s[0:1], 0x8
	s_load_dwordx2 s[18:19], s[0:1], 0x18
	v_mov_b32_e32 v11, 0
	v_lshlrev_b32_e32 v10, 2, v0
	v_readfirstlane_b32 s26, v0
	s_mov_b64 s[4:5], 0x3000000
	s_mov_b64 s[6:7], 0x1234
	s_waitcnt lgkmcnt(0)
	v_lshl_add_u64 v[2:3], s[20:21], 0, v[10:11]
	v_lshl_add_u64 v[6:7], v[2:3], 0, s[4:5]
	v_lshl_add_u64 v[18:19], v[6:7], 0, s[6:7]
	v_cmp_gt_u32_e64 s[12:13], 20, v0
	global_load_dword v3, v[6:7], off
	global_load_dword v2, v[6:7], off offset:1104
	global_load_dword v8, v[6:7], off offset:2208
	global_load_dword v9, v[6:7], off offset:3312
	global_load_dword v10, v[18:19], off offset:-244
	global_load_dword v12, v[18:19], off offset:860
	global_load_dword v13, v[18:19], off offset:1964
	global_load_dword v14, v[18:19], off offset:3068
	v_mov_b32_e32 v5, 0
	v_mov_b32_e32 v1, 0
	v_mov_b32_e32 v4, 0
	v_mov_b32_e32 v15, 0
	v_mov_b32_e32 v16, 0
	v_mov_b32_e32 v17, 0
	v_mov_b32_e32 v21, 0
	s_and_saveexec_b64 s[4:5], s[12:13]
	global_load_dword v5, v[6:7], off offset:1024
	global_load_dword v11, v[6:7], off offset:2128
	global_load_dword v4, v[6:7], off offset:3232
	global_load_dword v1, v[18:19], off offset:-324
	global_load_dword v16, v[18:19], off offset:780
	global_load_dword v15, v[18:19], off offset:1884
	global_load_dword v21, v[18:19], off offset:2988
	global_load_dword v17, v[18:19], off offset:4092
.LBB3_16:
	s_or_b64 exec, exec, s[4:5]
	v_and_b32_e32 v92, 63, v0
	s_lshr_b32 s27, s26, 6
	v_lshlrev_b32_e32 v30, 2, v0
	v_mov_b32_e32 v31, -1
	v_mov_b32_e32 v34, 0
	v_cmp_gt_u32_e64 s[14:15], 12, v0
	s_and_saveexec_b64 s[16:17], s[14:15]
	ds_write_b32 v30, v31 offset:54144
	s_mov_b64 exec, s[16:17]
	s_waitcnt vmcnt(0)
	v_add_u32_e32 v42, v2, v3
	v_add_u32_e32 v52, v11, v5
	v_add_u32_e32 v43, v8, v42
	v_add_u32_e32 v53, v4, v52
	v_add_u32_e32 v44, v9, v43
	v_add_u32_e32 v54, v1, v53
	v_add_u32_e32 v45, v10, v44
	v_add_u32_e32 v55, v16, v54
	v_add_u32_e32 v46, v12, v45
	v_add_u32_e32 v56, v15, v55
	v_add_u32_e32 v47, v13, v46
	v_add_u32_e32 v57, v21, v56
	v_add_u32_e32 v48, v14, v47
	v_add_u32_e32 v58, v17, v57
	v_add_u32_e32 v49, 0x7f, v48
	v_add_u32_e32 v59, 0x7f, v58
	v_lshrrev_b32_e32 v49, 7, v49
	v_lshrrev_b32_e32 v59, 7, v59
	v_mov_b32_e32 v50, v49
	v_mov_b32_e32 v51, v59
	s_nop 0
	v_add_u32_dpp v50, v50, v50 row_shr:1 row_mask:0xf bank_mask:0xf
	v_add_u32_dpp v51, v51, v51 row_shr:1 row_mask:0xf bank_mask:0xf
	s_nop 0
	v_add_u32_dpp v50, v50, v50 row_shr:2 row_mask:0xf bank_mask:0xf
	v_add_u32_dpp v51, v51, v51 row_shr:2 row_mask:0xf bank_mask:0xf
	s_nop 0
	v_add_u32_dpp v50, v50, v50 row_shr:4 row_mask:0xf bank_mask:0xf
	v_add_u32_dpp v51, v51, v51 row_shr:4 row_mask:0xf bank_mask:0xf
	s_nop 0
	v_add_u32_dpp v50, v50, v50 row_shr:8 row_mask:0xf bank_mask:0xf
	v_add_u32_dpp v51, v51, v51 row_shr:8 row_mask:0xf bank_mask:0xf
	s_nop 0
	v_add_u32_dpp v50, v50, v50 row_bcast:15 row_mask:0xa bank_mask:0xf
	v_add_u32_dpp v51, v51, v51 row_bcast:15 row_mask:0xa bank_mask:0xf
	s_nop 0
	v_add_u32_dpp v50, v50, v50 row_bcast:31 row_mask:0xc bank_mask:0xf
	v_add_u32_dpp v51, v51, v51 row_bcast:31 row_mask:0xc bank_mask:0xf
	s_nop 0
	v_readlane_b32 s6, v50, 63
	s_lshl_b32 s7, s27, 2
	v_mov_b32_e32 v33, s7
	v_cmp_eq_u32_e64 s[14:15], 0, v92
	v_mov_b32_e32 v32, s6
	s_and_saveexec_b64 s[16:17], s[14:15]
	ds_write_b32 v33, v32 offset:54192
	s_mov_b64 exec, s[16:17]
	s_waitcnt lgkmcnt(0)
	s_barrier
	ds_read_b128 v[64:67], v34 offset:54192
	s_waitcnt lgkmcnt(0)
	v_readfirstlane_b32 s6, v64
	v_readfirstlane_b32 s7, v65
	v_readfirstlane_b32 s8, v66
	v_readfirstlane_b32 s9, v67
	s_nop 3
	s_add_u32 s10, s6, s7
	s_add_u32 s10, s10, s8
	s_add_u32 s10, s10, s9
	s_cmp_gt_u32 s27, 0
	s_cselect_b32 s14, s6, 0
	s_cmp_gt_u32 s27, 1
	s_cselect_b32 s15, s7, 0
	s_cmp_gt_u32 s27, 2
	s_cselect_b32 s16, s8, 0
	s_add_u32 s11, s14, s15
	s_add_u32 s11, s11, s16
	v_sub_u32_e32 v68, v50, v49
	v_sub_u32_e32 v69, v51, v59
	v_add_u32_e32 v68, s11, v68
	v_add_u32_e32 v69, s10, v69
	v_add_u32_e32 v70, v68, v49
	v_add_u32_e32 v71, v69, v59
	v_mov_b32_e32 v36, v0
	v_sub_u32_e32 v37, s2, v68
	v_mov_b32_e32 v38, v48
	v_mov_b32_e32 v39, v3
	v_or_b32_e32 v60, 0x100, v0
	v_sub_u32_e32 v61, s2, v69
	v_mov_b32_e32 v62, v58
	v_mov_b32_e32 v63, v5
	v_cmp_ge_u32_e64 s[14:15], s2, v68
	v_cmp_lt_u32_e64 s[16:17], s2, v70
	v_cmp_ge_u32_e64 s[6:7], s2, v69
	v_cmp_lt_u32_e64 s[8:9], s2, v71
	s_and_b64 s[14:15], s[14:15], s[16:17]
	s_and_b64 s[6:7], s[6:7], s[8:9]
	s_and_saveexec_b64 s[16:17], s[14:15]
	ds_write_b128 v34, v[36:39] offset:54144
	ds_write_b128 v34, v[42:45] offset:54160
	ds_write_b96 v34, v[46:48] offset:54176
	s_mov_b64 exec, s[16:17]
	s_and_saveexec_b64 s[16:17], s[6:7]
	ds_write_b128 v34, v[60:63] offset:54144
	ds_write_b128 v34, v[52:55] offset:54160
	ds_write_b96 v34, v[56:58] offset:54176
	s_mov_b64 exec, s[16:17]
	v_mov_b32_e32 v1, 0
	s_waitcnt lgkmcnt(0)
	s_barrier
	ds_read_b32 v2, v1 offset:54144
	s_waitcnt lgkmcnt(0)
	v_cmp_gt_i32_e32 vcc, 0, v2
	v_readfirstlane_b32 s2, v2
	s_cbranch_vccnz .LBB3_39
	v_mov_b32_e32 v5, 0xd39c
	v_mov_b32_e32 v2, 0xd384
	v_mov_b32_e32 v3, 0xd38c
	v_mov_b32_e32 v4, 0xd394
	ds_read2_b32 v[8:9], v5 offset1:1
	ds_read2_b32 v[6:7], v2 offset1:1
	ds_read2_b32 v[12:13], v3 offset1:1
	ds_read2_b32 v[10:11], v4 offset1:1
	ds_read_b32 v1, v1 offset:54180
	s_mov_b32 s28, 0
	s_cmp_lt_u32 s2, 23
	s_mov_b32 s0, s2
	s_cbranch_scc1 .LBB3_29
	s_movk_i32 s4, 0xffe8
	s_mov_b32 s1, 22
	s_mov_b32 s0, s2

.LBB3_35:
	s_andn2_b64 vcc, exec, s[2:3]
	s_cbranch_vccnz .LBB3_39
	s_waitcnt vmcnt(4)
	v_ashrrev_i32_e32 v81, 31, v80
	v_lshl_add_u64 v[2:3], v[80:81], 3, s[20:21]
	v_add_co_u32_e32 v2, vcc, 0x48000, v2
	s_movk_i32 s8, 0x620
	s_nop 0
	v_addc_co_u32_e32 v3, vcc, 0, v3, vcc
	global_load_dwordx2 v[82:83], v[2:3], off
	v_and_b32_e32 v2, 0x70, v7
	v_bitop3_b32 v2, v0, v2, 48 bitop3:0x6c
	s_waitcnt vmcnt(4)
	v_mad_u64_u32 v[64:65], s[6:7], v9, s8, v[2:3]
	v_lshrrev_b32_e32 v3, 4, v92
	v_bitop3_b32 v3, v3, v0, 4 bitop3:0x36
	v_lshlrev_b32_e32 v3, 4, v3
	v_and_b32_e32 v4, 0x70, v3
	s_waitcnt vmcnt(3)
	v_mad_u64_u32 v[66:67], s[6:7], v8, s8, v[4:5]
	s_waitcnt vmcnt(2)
	v_mad_u64_u32 v[68:69], s[6:7], v6, s8, v[2:3]
	s_waitcnt vmcnt(1)
	v_mad_u64_u32 v[70:71], s[6:7], v1, s8, v[4:5]
	v_lshrrev_b32_e32 v85, 5, v92
	v_bfe_u32 v2, v0, 1, 3
	s_mov_b64 s[6:7], 0x1800
	s_add_u32 s4, s20, 0x4000000
	v_bitop3_b32 v32, v85, v2, 2 bitop3:0x36
	v_bitop3_b32 v33, v85, v2, 4 bitop3:0x36
	v_bitop3_b32 v34, v85, v2, 6 bitop3:0x36
	v_lshl_add_u64 v[2:3], v[86:87], 0, s[6:7]
	s_addc_u32 s5, s21, 0
	global_load_dwordx4 v[116:119], v64, s[4:5] offset:0
	global_load_dwordx4 v[120:123], v66, s[4:5] offset:0
	global_load_dwordx4 v[124:127], v68, s[4:5] offset:0
	global_load_dwordx4 v[128:131], v70, s[4:5] offset:0
	global_load_dwordx4 v[132:135], v64, s[4:5] offset:128
	global_load_dwordx4 v[136:139], v66, s[4:5] offset:128
	global_load_dwordx4 v[140:143], v68, s[4:5] offset:128
	global_load_dwordx4 v[144:147], v70, s[4:5] offset:128
	global_load_dwordx4 v[148:151], v64, s[4:5] offset:256
	global_load_dwordx4 v[152:155], v66, s[4:5] offset:256
	global_load_dwordx4 v[156:159], v68, s[4:5] offset:256
	global_load_dwordx4 v[72:75], v70, s[4:5] offset:256
	s_lshl_b32 s2, s27, 12
	s_addk_i32 s2, 0x6000
	v_lshrrev_b32_e32 v1, 1, v0
	v_or_b32_e32 v81, s2, v84
	v_lshlrev_b32_e32 v0, 7, v0
	v_and_b32_e32 v8, 0xf80, v0
	v_lshlrev_b32_e32 v9, 4, v32
	v_bitop3_b32 v1, v85, v1, 7 bitop3:0x78
	v_or3_b32 v96, s2, v9, v8
	v_lshlrev_b32_e32 v9, 4, v33
	v_lshlrev_b32_e32 v1, 4, v1
	v_or3_b32 v97, s2, v9, v8
	v_lshlrev_b32_e32 v9, 4, v34
	v_or3_b32 v95, s2, v1, v8
	v_or3_b32 v94, s2, v9, v8
	v_add_u32_e32 v98, 0x103c0, v84
	s_add_u32 m0, s46, 0x0
	s_nop 0
	global_load_lds_dwordx4 v76, s[40:41]
	s_add_u32 m0, s47, 0x0
	s_nop 0
	global_load_lds_dwordx4 v77, s[42:43]
	s_add_u32 m0, s48, 0x0
	s_nop 0
	global_load_lds_dwordx4 v78, s[44:45]
	s_add_u32 m0, s46, 0x3000
	s_add_u32 s40, s40, 0x1800
	s_addc_u32 s41, s41, 0
	global_load_lds_dwordx4 v76, s[40:41]
	s_add_u32 m0, s47, 0x3000
	s_add_u32 s42, s42, 0x1800
	s_addc_u32 s43, s43, 0
	global_load_lds_dwordx4 v77, s[42:43]
	s_add_u32 m0, s48, 0x3000
	s_add_u32 s44, s44, 0x1800
	s_addc_u32 s45, s45, 0
	global_load_lds_dwordx4 v78, s[44:45]
	s_add_u32 m0, s46, 0xd3c0
	s_add_u32 s40, s40, 0x1800
	s_addc_u32 s41, s41, 0
	global_load_lds_dwordx4 v76, s[40:41]
	s_add_u32 m0, s47, 0xd3c0
	s_add_u32 s42, s42, 0x1800
	s_addc_u32 s43, s43, 0
	global_load_lds_dwordx4 v77, s[42:43]
	s_add_u32 m0, s48, 0xd3c0
	s_add_u32 s44, s44, 0x1800
	s_addc_u32 s45, s45, 0
	global_load_lds_dwordx4 v78, s[44:45]
	s_add_u32 m0, s46, 0x103c0
	s_add_u32 s40, s40, 0x1800
	s_addc_u32 s41, s41, 0
	global_load_lds_dwordx4 v76, s[40:41]
	s_add_u32 m0, s47, 0x103c0
	s_add_u32 s42, s42, 0x1800
	s_addc_u32 s43, s43, 0
	global_load_lds_dwordx4 v77, s[42:43]
	s_add_u32 m0, s48, 0x103c0
	s_add_u32 s44, s44, 0x1800
	s_addc_u32 s45, s45, 0
	global_load_lds_dwordx4 v78, s[44:45]
	s_waitcnt vmcnt(20)
	ds_write_b128 v81, v[116:119]
	ds_write_b128 v81, v[120:123] offset:1024
	ds_write_b128 v81, v[124:127] offset:2048
	ds_write_b128 v81, v[128:131] offset:3072
	ds_read_b128 v[52:55], v95
	ds_read_b128 v[56:59], v96
	ds_read_b128 v[60:63], v97
	ds_read_b128 v[0:3], v94
	global_load_dwordx4 v[116:119], v64, s[4:5] offset:384
	global_load_dwordx4 v[120:123], v66, s[4:5] offset:384
	global_load_dwordx4 v[124:127], v68, s[4:5] offset:384
	global_load_dwordx4 v[128:131], v70, s[4:5] offset:384
	s_waitcnt vmcnt(13)
	s_waitcnt lgkmcnt(0)
	s_barrier
	ds_read_b128 v[4:7], v84 offset:0
	ds_read_b128 v[8:11], v84 offset:1024
	ds_read_b128 v[12:15], v84 offset:2048
	ds_read_b128 v[16:19], v84 offset:3072
	ds_read_b128 v[20:23], v84 offset:4096
	ds_read_b128 v[24:27], v84 offset:5120
	ds_read_b128 v[28:31], v84 offset:6144
	ds_read_b128 v[32:35], v84 offset:7168
	ds_read_b128 v[36:39], v84 offset:8192
	ds_read_b128 v[40:43], v84 offset:9216
	ds_read_b128 v[44:47], v84 offset:10240
	ds_read_b128 v[48:51], v84 offset:11264
	s_waitcnt lgkmcnt(6)
	v_mfma_f32_32x32x16_f16 a[80:95], v[4:7], v[52:55], 0
	v_mfma_f32_32x32x16_f16 a[64:79], v[8:11], v[52:55], 0
	v_mfma_f32_32x32x16_f16 a[48:63], v[12:15], v[52:55], 0
	s_waitcnt vmcnt(10)
	s_waitcnt lgkmcnt(0)
	s_barrier
	ds_read_b128 v[4:7], v84 offset:12288
	ds_read_b128 v[8:11], v84 offset:13312
	ds_read_b128 v[12:15], v84 offset:14336
	v_mfma_f32_32x32x16_f16 a[32:47], v[16:19], v[52:55], 0
	ds_read_b128 v[16:19], v84 offset:15360
	v_mfma_f32_32x32x16_f16 a[16:31], v[20:23], v[52:55], 0
	ds_read_b128 v[20:23], v84 offset:16384
	v_mfma_f32_32x32x16_f16 a[0:15], v[24:27], v[52:55], 0
	ds_read_b128 v[24:27], v84 offset:17408
	v_mfma_f32_32x32x16_f16 a[80:95], v[28:31], v[56:59], a[80:95]
	s_add_u32 m0, s46, 0x0
	s_add_u32 s40, s40, 0x1800
	s_addc_u32 s41, s41, 0
	global_load_lds_dwordx4 v76, s[40:41]
	ds_read_b128 v[28:31], v84 offset:18432
	v_mfma_f32_32x32x16_f16 a[64:79], v[32:35], v[56:59], a[64:79]
	ds_read_b128 v[32:35], v84 offset:19456
	v_mfma_f32_32x32x16_f16 a[48:63], v[36:39], v[56:59], a[48:63]
	s_add_u32 m0, s47, 0x0
	s_add_u32 s42, s42, 0x1800
	s_addc_u32 s43, s43, 0
	global_load_lds_dwordx4 v77, s[42:43]
	ds_read_b128 v[36:39], v84 offset:20480
	v_mfma_f32_32x32x16_f16 a[32:47], v[40:43], v[56:59], a[32:47]
	ds_read_b128 v[40:43], v84 offset:21504
	v_mfma_f32_32x32x16_f16 a[16:31], v[44:47], v[56:59], a[16:31]
	s_add_u32 m0, s48, 0x0
	s_add_u32 s44, s44, 0x1800
	s_addc_u32 s45, s45, 0
	global_load_lds_dwordx4 v78, s[44:45]
	ds_read_b128 v[44:47], v84 offset:22528
	v_mfma_f32_32x32x16_f16 a[0:15], v[48:51], v[56:59], a[0:15]
	ds_read_b128 v[48:51], v84 offset:23552
	s_waitcnt lgkmcnt(6)
	v_mfma_f32_32x32x16_f16 a[80:95], v[4:7], v[60:63], a[80:95]
	s_waitcnt vmcnt(23)
	ds_write_b128 v81, v[132:135]
	ds_write_b128 v81, v[136:139] offset:1024
	v_mfma_f32_32x32x16_f16 a[64:79], v[8:11], v[60:63], a[64:79]
	ds_write_b128 v81, v[140:143] offset:2048
	ds_write_b128 v81, v[144:147] offset:3072
	v_mfma_f32_32x32x16_f16 a[48:63], v[12:15], v[60:63], a[48:63]
	ds_read_b128 v[100:103], v95
	ds_read_b128 v[104:107], v96
	ds_read_b128 v[108:111], v97
	ds_read_b128 v[112:115], v94
	s_waitcnt vmcnt(10)
	s_waitcnt lgkmcnt(8)
	s_barrier
	ds_read_b128 v[4:7], v84 offset:54208
	ds_read_b128 v[8:11], v84 offset:55232
	ds_read_b128 v[12:15], v84 offset:56256
	v_mfma_f32_32x32x16_f16 a[32:47], v[16:19], v[60:63], a[32:47]
	ds_read_b128 v[16:19], v84 offset:57280
	v_mfma_f32_32x32x16_f16 a[16:31], v[20:23], v[60:63], a[16:31]
	ds_read_b128 v[20:23], v84 offset:58304
	v_mfma_f32_32x32x16_f16 a[0:15], v[24:27], v[60:63], a[0:15]
	ds_read_b128 v[24:27], v84 offset:59328
	s_waitcnt lgkmcnt(6)
	v_mfma_f32_32x32x16_f16 a[80:95], v[28:31], v[0:3], a[80:95]
	s_add_u32 m0, s46, 0x3000
	s_add_u32 s40, s40, 0x1800
	s_addc_u32 s41, s41, 0
	global_load_lds_dwordx4 v76, s[40:41]
	ds_read_b128 v[28:31], v84 offset:60352
	v_mfma_f32_32x32x16_f16 a[64:79], v[32:35], v[0:3], a[64:79]
	global_load_dwordx4 v[132:135], v64, s[4:5] offset:512
	global_load_dwordx4 v[136:139], v66, s[4:5] offset:512
	ds_read_b128 v[32:35], v84 offset:61376
	v_mfma_f32_32x32x16_f16 a[48:63], v[36:39], v[0:3], a[48:63]
	s_add_u32 m0, s47, 0x3000
	s_add_u32 s42, s42, 0x1800
	s_addc_u32 s43, s43, 0
	global_load_lds_dwordx4 v77, s[42:43]
	ds_read_b128 v[36:39], v84 offset:62400
	v_mfma_f32_32x32x16_f16 a[32:47], v[40:43], v[0:3], a[32:47]
	global_load_dwordx4 v[140:143], v68, s[4:5] offset:512
	global_load_dwordx4 v[144:147], v70, s[4:5] offset:512
	ds_read_b128 v[40:43], v84 offset:63424
	v_mfma_f32_32x32x16_f16 a[16:31], v[44:47], v[0:3], a[16:31]
	s_add_u32 m0, s48, 0x3000
	s_add_u32 s44, s44, 0x1800
	s_addc_u32 s45, s45, 0
	global_load_lds_dwordx4 v78, s[44:45]
	ds_read_b128 v[44:47], v84 offset:64448
	v_mfma_f32_32x32x16_f16 a[0:15], v[48:51], v[0:3], a[0:15]
	ds_read_b128 v[48:51], v84 offset:65472
	s_waitcnt lgkmcnt(6)
	v_mfma_f32_32x32x16_f16 a[80:95], v[4:7], v[100:103], a[80:95]
	v_mfma_f32_32x32x16_f16 a[64:79], v[8:11], v[100:103], a[64:79]
	v_mfma_f32_32x32x16_f16 a[48:63], v[12:15], v[100:103], a[48:63]
	s_waitcnt vmcnt(14)
	s_waitcnt lgkmcnt(0)
	s_barrier
	ds_read_b128 v[4:7], v98
	ds_read_b128 v[8:11], v98 offset:1024
	ds_read_b128 v[12:15], v98 offset:2048
	v_mfma_f32_32x32x16_f16 a[32:47], v[16:19], v[100:103], a[32:47]
	ds_read_b128 v[16:19], v98 offset:3072
	v_mfma_f32_32x32x16_f16 a[16:31], v[20:23], v[100:103], a[16:31]
	ds_read_b128 v[20:23], v98 offset:4096
	v_mfma_f32_32x32x16_f16 a[0:15], v[24:27], v[100:103], a[0:15]
	ds_read_b128 v[24:27], v98 offset:5120
	v_mfma_f32_32x32x16_f16 a[80:95], v[28:31], v[104:107], a[80:95]
	s_add_u32 m0, s46, 0xd3c0
	s_add_u32 s40, s40, 0x1800
	s_addc_u32 s41, s41, 0
	global_load_lds_dwordx4 v76, s[40:41]
	ds_read_b128 v[28:31], v98 offset:6144
	v_mfma_f32_32x32x16_f16 a[64:79], v[32:35], v[104:107], a[64:79]
	ds_read_b128 v[32:35], v98 offset:7168
	v_mfma_f32_32x32x16_f16 a[48:63], v[36:39], v[104:107], a[48:63]
	s_add_u32 m0, s47, 0xd3c0
	s_add_u32 s42, s42, 0x1800
	s_addc_u32 s43, s43, 0
	global_load_lds_dwordx4 v77, s[42:43]
	ds_read_b128 v[36:39], v98 offset:8192
	v_mfma_f32_32x32x16_f16 a[32:47], v[40:43], v[104:107], a[32:47]
	ds_read_b128 v[40:43], v98 offset:9216
	v_mfma_f32_32x32x16_f16 a[16:31], v[44:47], v[104:107], a[16:31]
	s_add_u32 m0, s48, 0xd3c0
	s_add_u32 s44, s44, 0x1800
	s_addc_u32 s45, s45, 0
	global_load_lds_dwordx4 v78, s[44:45]
	ds_read_b128 v[44:47], v98 offset:10240
	v_mfma_f32_32x32x16_f16 a[0:15], v[48:51], v[104:107], a[0:15]
	ds_read_b128 v[48:51], v98 offset:11264
	s_waitcnt lgkmcnt(6)
	v_mfma_f32_32x32x16_f16 a[80:95], v[4:7], v[108:111], a[80:95]
	s_waitcnt vmcnt(29)
	ds_write_b128 v81, v[148:151]
	ds_write_b128 v81, v[152:155] offset:1024
	v_mfma_f32_32x32x16_f16 a[64:79], v[8:11], v[108:111], a[64:79]
	ds_write_b128 v81, v[156:159] offset:2048
	ds_write_b128 v81, v[72:75] offset:3072
	v_mfma_f32_32x32x16_f16 a[48:63], v[12:15], v[108:111], a[48:63]
	ds_read_b128 v[52:55], v95
	ds_read_b128 v[56:59], v96
	ds_read_b128 v[60:63], v97
	ds_read_b128 v[0:3], v94
	s_waitcnt vmcnt(10)
	s_waitcnt lgkmcnt(8)
	s_barrier
	ds_read_b128 v[4:7], v84 offset:0
	ds_read_b128 v[8:11], v84 offset:1024
	ds_read_b128 v[12:15], v84 offset:2048
	v_mfma_f32_32x32x16_f16 a[32:47], v[16:19], v[108:111], a[32:47]
	ds_read_b128 v[16:19], v84 offset:3072
	v_mfma_f32_32x32x16_f16 a[16:31], v[20:23], v[108:111], a[16:31]
	ds_read_b128 v[20:23], v84 offset:4096
	v_mfma_f32_32x32x16_f16 a[0:15], v[24:27], v[108:111], a[0:15]
	ds_read_b128 v[24:27], v84 offset:5120
	s_waitcnt lgkmcnt(6)
	v_mfma_f32_32x32x16_f16 a[80:95], v[28:31], v[112:115], a[80:95]
	s_add_u32 m0, s46, 0x103c0
	s_add_u32 s40, s40, 0x1800
	s_addc_u32 s41, s41, 0
	global_load_lds_dwordx4 v76, s[40:41]
	ds_read_b128 v[28:31], v84 offset:6144
	v_mfma_f32_32x32x16_f16 a[64:79], v[32:35], v[112:115], a[64:79]
	global_load_dwordx4 v[148:151], v64, s[4:5] offset:640
	global_load_dwordx4 v[152:155], v66, s[4:5] offset:640
	ds_read_b128 v[32:35], v84 offset:7168
	v_mfma_f32_32x32x16_f16 a[48:63], v[36:39], v[112:115], a[48:63]
	s_add_u32 m0, s47, 0x103c0
	s_add_u32 s42, s42, 0x1800
	s_addc_u32 s43, s43, 0
	global_load_lds_dwordx4 v77, s[42:43]
	ds_read_b128 v[36:39], v84 offset:8192
	v_mfma_f32_32x32x16_f16 a[32:47], v[40:43], v[112:115], a[32:47]
	global_load_dwordx4 v[156:159], v68, s[4:5] offset:640
	global_load_dwordx4 v[72:75], v70, s[4:5] offset:640
	ds_read_b128 v[40:43], v84 offset:9216
	v_mfma_f32_32x32x16_f16 a[16:31], v[44:47], v[112:115], a[16:31]
	s_add_u32 m0, s48, 0x103c0
	s_add_u32 s44, s44, 0x1800
	s_addc_u32 s45, s45, 0
	global_load_lds_dwordx4 v78, s[44:45]
	ds_read_b128 v[44:47], v84 offset:10240
	v_mfma_f32_32x32x16_f16 a[0:15], v[48:51], v[112:115], a[0:15]
	ds_read_b128 v[48:51], v84 offset:11264
	s_waitcnt lgkmcnt(6)
	v_mfma_f32_32x32x16_f16 a[80:95], v[4:7], v[52:55], a[80:95]
	v_mfma_f32_32x32x16_f16 a[64:79], v[8:11], v[52:55], a[64:79]
	v_mfma_f32_32x32x16_f16 a[48:63], v[12:15], v[52:55], a[48:63]
	s_waitcnt vmcnt(10)
	s_waitcnt lgkmcnt(0)
	s_barrier
	ds_read_b128 v[4:7], v84 offset:12288
	ds_read_b128 v[8:11], v84 offset:13312
	ds_read_b128 v[12:15], v84 offset:14336
	v_mfma_f32_32x32x16_f16 a[32:47], v[16:19], v[52:55], a[32:47]
	ds_read_b128 v[16:19], v84 offset:15360
	v_mfma_f32_32x32x16_f16 a[16:31], v[20:23], v[52:55], a[16:31]
	ds_read_b128 v[20:23], v84 offset:16384
	v_mfma_f32_32x32x16_f16 a[0:15], v[24:27], v[52:55], a[0:15]
	ds_read_b128 v[24:27], v84 offset:17408
	v_mfma_f32_32x32x16_f16 a[80:95], v[28:31], v[56:59], a[80:95]
	s_add_u32 m0, s46, 0x0
	s_add_u32 s40, s40, 0x1800
	s_addc_u32 s41, s41, 0
	global_load_lds_dwordx4 v76, s[40:41]
	ds_read_b128 v[28:31], v84 offset:18432
	v_mfma_f32_32x32x16_f16 a[64:79], v[32:35], v[56:59], a[64:79]
	ds_read_b128 v[32:35], v84 offset:19456
	v_mfma_f32_32x32x16_f16 a[48:63], v[36:39], v[56:59], a[48:63]
	s_add_u32 m0, s47, 0x0
	s_add_u32 s42, s42, 0x1800
	s_addc_u32 s43, s43, 0
	global_load_lds_dwordx4 v77, s[42:43]
	ds_read_b128 v[36:39], v84 offset:20480
	v_mfma_f32_32x32x16_f16 a[32:47], v[40:43], v[56:59], a[32:47]
	ds_read_b128 v[40:43], v84 offset:21504
	v_mfma_f32_32x32x16_f16 a[16:31], v[44:47], v[56:59], a[16:31]
	s_add_u32 m0, s48, 0x0
	s_add_u32 s44, s44, 0x1800
	s_addc_u32 s45, s45, 0
	global_load_lds_dwordx4 v78, s[44:45]
	ds_read_b128 v[44:47], v84 offset:22528
	v_mfma_f32_32x32x16_f16 a[0:15], v[48:51], v[56:59], a[0:15]
	ds_read_b128 v[48:51], v84 offset:23552
	s_waitcnt lgkmcnt(6)
	v_mfma_f32_32x32x16_f16 a[80:95], v[4:7], v[60:63], a[80:95]
	s_waitcnt vmcnt(23)
	ds_write_b128 v81, v[116:119]
	ds_write_b128 v81, v[120:123] offset:1024
	v_mfma_f32_32x32x16_f16 a[64:79], v[8:11], v[60:63], a[64:79]
	ds_write_b128 v81, v[124:127] offset:2048
	ds_write_b128 v81, v[128:131] offset:3072
	v_mfma_f32_32x32x16_f16 a[48:63], v[12:15], v[60:63], a[48:63]
	ds_read_b128 v[100:103], v95
	ds_read_b128 v[104:107], v96
	ds_read_b128 v[108:111], v97
	ds_read_b128 v[112:115], v94
	s_waitcnt vmcnt(10)
	s_waitcnt lgkmcnt(8)
	s_barrier
	ds_read_b128 v[4:7], v84 offset:54208
	ds_read_b128 v[8:11], v84 offset:55232
	ds_read_b128 v[12:15], v84 offset:56256
	v_mfma_f32_32x32x16_f16 a[32:47], v[16:19], v[60:63], a[32:47]
	ds_read_b128 v[16:19], v84 offset:57280
	v_mfma_f32_32x32x16_f16 a[16:31], v[20:23], v[60:63], a[16:31]
	ds_read_b128 v[20:23], v84 offset:58304
	v_mfma_f32_32x32x16_f16 a[0:15], v[24:27], v[60:63], a[0:15]
	ds_read_b128 v[24:27], v84 offset:59328
	s_waitcnt lgkmcnt(6)
	v_mfma_f32_32x32x16_f16 a[80:95], v[28:31], v[0:3], a[80:95]
	s_add_u32 m0, s46, 0x3000
	s_add_u32 s40, s40, 0x1800
	s_addc_u32 s41, s41, 0
	global_load_lds_dwordx4 v76, s[40:41]
	ds_read_b128 v[28:31], v84 offset:60352
	v_mfma_f32_32x32x16_f16 a[64:79], v[32:35], v[0:3], a[64:79]
	global_load_dwordx4 v[116:119], v64, s[4:5] offset:768
	global_load_dwordx4 v[120:123], v66, s[4:5] offset:768
	ds_read_b128 v[32:35], v84 offset:61376
	v_mfma_f32_32x32x16_f16 a[48:63], v[36:39], v[0:3], a[48:63]
	s_add_u32 m0, s47, 0x3000
	s_add_u32 s42, s42, 0x1800
	s_addc_u32 s43, s43, 0
	global_load_lds_dwordx4 v77, s[42:43]
	ds_read_b128 v[36:39], v84 offset:62400
	v_mfma_f32_32x32x16_f16 a[32:47], v[40:43], v[0:3], a[32:47]
	global_load_dwordx4 v[124:127], v68, s[4:5] offset:768
	global_load_dwordx4 v[128:131], v70, s[4:5] offset:768
	ds_read_b128 v[40:43], v84 offset:63424
	v_mfma_f32_32x32x16_f16 a[16:31], v[44:47], v[0:3], a[16:31]
	s_add_u32 m0, s48, 0x3000
	s_add_u32 s44, s44, 0x1800
	s_addc_u32 s45, s45, 0
	global_load_lds_dwordx4 v78, s[44:45]
	ds_read_b128 v[44:47], v84 offset:64448
	v_mfma_f32_32x32x16_f16 a[0:15], v[48:51], v[0:3], a[0:15]
	ds_read_b128 v[48:51], v84 offset:65472
	s_waitcnt lgkmcnt(6)
	v_mfma_f32_32x32x16_f16 a[80:95], v[4:7], v[100:103], a[80:95]
	v_mfma_f32_32x32x16_f16 a[64:79], v[8:11], v[100:103], a[64:79]
	v_mfma_f32_32x32x16_f16 a[48:63], v[12:15], v[100:103], a[48:63]
	s_waitcnt vmcnt(10)
	s_waitcnt lgkmcnt(0)
	s_barrier
	ds_read_b128 v[4:7], v98
	ds_read_b128 v[8:11], v98 offset:1024
	ds_read_b128 v[12:15], v98 offset:2048
	v_mfma_f32_32x32x16_f16 a[32:47], v[16:19], v[100:103], a[32:47]
	ds_read_b128 v[16:19], v98 offset:3072
	v_mfma_f32_32x32x16_f16 a[16:31], v[20:23], v[100:103], a[16:31]
	ds_read_b128 v[20:23], v98 offset:4096
	v_mfma_f32_32x32x16_f16 a[0:15], v[24:27], v[100:103], a[0:15]
	ds_read_b128 v[24:27], v98 offset:5120
	v_mfma_f32_32x32x16_f16 a[80:95], v[28:31], v[104:107], a[80:95]
	s_add_u32 m0, s46, 0xd3c0
	s_add_u32 s40, s40, 0x1800
	s_addc_u32 s41, s41, 0
	global_load_lds_dwordx4 v76, s[40:41]
	ds_read_b128 v[28:31], v98 offset:6144
	v_mfma_f32_32x32x16_f16 a[64:79], v[32:35], v[104:107], a[64:79]
	ds_read_b128 v[32:35], v98 offset:7168
	v_mfma_f32_32x32x16_f16 a[48:63], v[36:39], v[104:107], a[48:63]
	s_add_u32 m0, s47, 0xd3c0
	s_add_u32 s42, s42, 0x1800
	s_addc_u32 s43, s43, 0
	global_load_lds_dwordx4 v77, s[42:43]
	ds_read_b128 v[36:39], v98 offset:8192
	v_mfma_f32_32x32x16_f16 a[32:47], v[40:43], v[104:107], a[32:47]
	ds_read_b128 v[40:43], v98 offset:9216
	v_mfma_f32_32x32x16_f16 a[16:31], v[44:47], v[104:107], a[16:31]
	s_add_u32 m0, s48, 0xd3c0
	s_add_u32 s44, s44, 0x1800
	s_addc_u32 s45, s45, 0
	global_load_lds_dwordx4 v78, s[44:45]
	ds_read_b128 v[44:47], v98 offset:10240
	v_mfma_f32_32x32x16_f16 a[0:15], v[48:51], v[104:107], a[0:15]
	ds_read_b128 v[48:51], v98 offset:11264
	s_waitcnt lgkmcnt(6)
	v_mfma_f32_32x32x16_f16 a[80:95], v[4:7], v[108:111], a[80:95]
	s_waitcnt vmcnt(24)
	ds_write_b128 v81, v[132:135]
	ds_write_b128 v81, v[136:139] offset:1024
	v_mfma_f32_32x32x16_f16 a[64:79], v[8:11], v[108:111], a[64:79]
	ds_write_b128 v81, v[140:143] offset:2048
	ds_write_b128 v81, v[144:147] offset:3072
	v_mfma_f32_32x32x16_f16 a[48:63], v[12:15], v[108:111], a[48:63]
	ds_read_b128 v[52:55], v95
	ds_read_b128 v[56:59], v96
	ds_read_b128 v[60:63], v97
	ds_read_b128 v[0:3], v94
	s_waitcnt vmcnt(10)
	s_waitcnt lgkmcnt(8)
	s_barrier
	ds_read_b128 v[4:7], v84 offset:0
	ds_read_b128 v[8:11], v84 offset:1024
	ds_read_b128 v[12:15], v84 offset:2048
	v_mfma_f32_32x32x16_f16 a[32:47], v[16:19], v[108:111], a[32:47]
	ds_read_b128 v[16:19], v84 offset:3072
	v_mfma_f32_32x32x16_f16 a[16:31], v[20:23], v[108:111], a[16:31]
	ds_read_b128 v[20:23], v84 offset:4096
	v_mfma_f32_32x32x16_f16 a[0:15], v[24:27], v[108:111], a[0:15]
	ds_read_b128 v[24:27], v84 offset:5120
	s_waitcnt lgkmcnt(6)
	v_mfma_f32_32x32x16_f16 a[80:95], v[28:31], v[112:115], a[80:95]
	s_add_u32 m0, s46, 0x103c0
	s_add_u32 s40, s40, 0x1800
	s_addc_u32 s41, s41, 0
	global_load_lds_dwordx4 v76, s[40:41]
	ds_read_b128 v[28:31], v84 offset:6144
	v_mfma_f32_32x32x16_f16 a[64:79], v[32:35], v[112:115], a[64:79]
	global_load_dwordx4 v[132:135], v64, s[4:5] offset:896
	global_load_dwordx4 v[136:139], v66, s[4:5] offset:896
	ds_read_b128 v[32:35], v84 offset:7168
	v_mfma_f32_32x32x16_f16 a[48:63], v[36:39], v[112:115], a[48:63]
	s_add_u32 m0, s47, 0x103c0
	s_add_u32 s42, s42, 0x1800
	s_addc_u32 s43, s43, 0
	global_load_lds_dwordx4 v77, s[42:43]
	ds_read_b128 v[36:39], v84 offset:8192
	v_mfma_f32_32x32x16_f16 a[32:47], v[40:43], v[112:115], a[32:47]
	global_load_dwordx4 v[140:143], v68, s[4:5] offset:896
	global_load_dwordx4 v[144:147], v70, s[4:5] offset:896
	ds_read_b128 v[40:43], v84 offset:9216
	v_mfma_f32_32x32x16_f16 a[16:31], v[44:47], v[112:115], a[16:31]
	s_add_u32 m0, s48, 0x103c0
	s_add_u32 s44, s44, 0x1800
	s_addc_u32 s45, s45, 0
	global_load_lds_dwordx4 v78, s[44:45]
	ds_read_b128 v[44:47], v84 offset:10240
	v_mfma_f32_32x32x16_f16 a[0:15], v[48:51], v[112:115], a[0:15]
	ds_read_b128 v[48:51], v84 offset:11264
	s_waitcnt lgkmcnt(6)
	v_mfma_f32_32x32x16_f16 a[80:95], v[4:7], v[52:55], a[80:95]
	v_mfma_f32_32x32x16_f16 a[64:79], v[8:11], v[52:55], a[64:79]
	v_mfma_f32_32x32x16_f16 a[48:63], v[12:15], v[52:55], a[48:63]
	s_waitcnt vmcnt(10)
	s_waitcnt lgkmcnt(0)
	s_barrier
	ds_read_b128 v[4:7], v84 offset:12288
	ds_read_b128 v[8:11], v84 offset:13312
	ds_read_b128 v[12:15], v84 offset:14336
	v_mfma_f32_32x32x16_f16 a[32:47], v[16:19], v[52:55], a[32:47]
	ds_read_b128 v[16:19], v84 offset:15360
	v_mfma_f32_32x32x16_f16 a[16:31], v[20:23], v[52:55], a[16:31]
	ds_read_b128 v[20:23], v84 offset:16384
	v_mfma_f32_32x32x16_f16 a[0:15], v[24:27], v[52:55], a[0:15]
	ds_read_b128 v[24:27], v84 offset:17408
	v_mfma_f32_32x32x16_f16 a[80:95], v[28:31], v[56:59], a[80:95]
	s_add_u32 m0, s46, 0x0
	s_add_u32 s40, s40, 0x1800
	s_addc_u32 s41, s41, 0
	global_load_lds_dwordx4 v76, s[40:41]
	ds_read_b128 v[28:31], v84 offset:18432
	v_mfma_f32_32x32x16_f16 a[64:79], v[32:35], v[56:59], a[64:79]
	ds_read_b128 v[32:35], v84 offset:19456
	v_mfma_f32_32x32x16_f16 a[48:63], v[36:39], v[56:59], a[48:63]
	s_add_u32 m0, s47, 0x0
	s_add_u32 s42, s42, 0x1800
	s_addc_u32 s43, s43, 0
	global_load_lds_dwordx4 v77, s[42:43]
	ds_read_b128 v[36:39], v84 offset:20480
	v_mfma_f32_32x32x16_f16 a[32:47], v[40:43], v[56:59], a[32:47]
	ds_read_b128 v[40:43], v84 offset:21504
	v_mfma_f32_32x32x16_f16 a[16:31], v[44:47], v[56:59], a[16:31]
	s_add_u32 m0, s48, 0x0
	s_add_u32 s44, s44, 0x1800
	s_addc_u32 s45, s45, 0
	global_load_lds_dwordx4 v78, s[44:45]
	ds_read_b128 v[44:47], v84 offset:22528
	v_mfma_f32_32x32x16_f16 a[0:15], v[48:51], v[56:59], a[0:15]
	ds_read_b128 v[48:51], v84 offset:23552
	s_waitcnt lgkmcnt(6)
	v_mfma_f32_32x32x16_f16 a[80:95], v[4:7], v[60:63], a[80:95]
	s_waitcnt vmcnt(24)
	ds_write_b128 v81, v[148:151]
	ds_write_b128 v81, v[152:155] offset:1024
	v_mfma_f32_32x32x16_f16 a[64:79], v[8:11], v[60:63], a[64:79]
	ds_write_b128 v81, v[156:159] offset:2048
	ds_write_b128 v81, v[72:75] offset:3072
	v_mfma_f32_32x32x16_f16 a[48:63], v[12:15], v[60:63], a[48:63]
	ds_read_b128 v[100:103], v95
	ds_read_b128 v[104:107], v96
	ds_read_b128 v[108:111], v97
	ds_read_b128 v[112:115], v94
	s_waitcnt vmcnt(10)
	s_waitcnt lgkmcnt(8)
	s_barrier
	ds_read_b128 v[4:7], v84 offset:54208
	ds_read_b128 v[8:11], v84 offset:55232
	ds_read_b128 v[12:15], v84 offset:56256
	v_mfma_f32_32x32x16_f16 a[32:47], v[16:19], v[60:63], a[32:47]
	ds_read_b128 v[16:19], v84 offset:57280
	v_mfma_f32_32x32x16_f16 a[16:31], v[20:23], v[60:63], a[16:31]
	ds_read_b128 v[20:23], v84 offset:58304
	v_mfma_f32_32x32x16_f16 a[0:15], v[24:27], v[60:63], a[0:15]
	ds_read_b128 v[24:27], v84 offset:59328
	s_waitcnt lgkmcnt(6)
	v_mfma_f32_32x32x16_f16 a[80:95], v[28:31], v[0:3], a[80:95]
	s_add_u32 m0, s46, 0x3000
	s_add_u32 s40, s40, 0x1800
	s_addc_u32 s41, s41, 0
	global_load_lds_dwordx4 v76, s[40:41]
	ds_read_b128 v[28:31], v84 offset:60352
	v_mfma_f32_32x32x16_f16 a[64:79], v[32:35], v[0:3], a[64:79]
	global_load_dwordx4 v[148:151], v64, s[4:5] offset:1024
	global_load_dwordx4 v[152:155], v66, s[4:5] offset:1024
	ds_read_b128 v[32:35], v84 offset:61376
	v_mfma_f32_32x32x16_f16 a[48:63], v[36:39], v[0:3], a[48:63]
	s_add_u32 m0, s47, 0x3000
	s_add_u32 s42, s42, 0x1800
	s_addc_u32 s43, s43, 0
	global_load_lds_dwordx4 v77, s[42:43]
	ds_read_b128 v[36:39], v84 offset:62400
	v_mfma_f32_32x32x16_f16 a[32:47], v[40:43], v[0:3], a[32:47]
	global_load_dwordx4 v[156:159], v68, s[4:5] offset:1024
	global_load_dwordx4 v[72:75], v70, s[4:5] offset:1024
	ds_read_b128 v[40:43], v84 offset:63424
	v_mfma_f32_32x32x16_f16 a[16:31], v[44:47], v[0:3], a[16:31]
	s_add_u32 m0, s48, 0x3000
	s_add_u32 s44, s44, 0x1800
	s_addc_u32 s45, s45, 0
	global_load_lds_dwordx4 v78, s[44:45]
	ds_read_b128 v[44:47], v84 offset:64448
	v_mfma_f32_32x32x16_f16 a[0:15], v[48:51], v[0:3], a[0:15]
	ds_read_b128 v[48:51], v84 offset:65472
	s_waitcnt lgkmcnt(6)
	v_mfma_f32_32x32x16_f16 a[80:95], v[4:7], v[100:103], a[80:95]
	v_mfma_f32_32x32x16_f16 a[64:79], v[8:11], v[100:103], a[64:79]
	v_mfma_f32_32x32x16_f16 a[48:63], v[12:15], v[100:103], a[48:63]
	s_waitcnt vmcnt(10)
	s_waitcnt lgkmcnt(0)
	s_barrier
	ds_read_b128 v[4:7], v98
	ds_read_b128 v[8:11], v98 offset:1024
	ds_read_b128 v[12:15], v98 offset:2048
	v_mfma_f32_32x32x16_f16 a[32:47], v[16:19], v[100:103], a[32:47]
	ds_read_b128 v[16:19], v98 offset:3072
	v_mfma_f32_32x32x16_f16 a[16:31], v[20:23], v[100:103], a[16:31]
	ds_read_b128 v[20:23], v98 offset:4096
	v_mfma_f32_32x32x16_f16 a[0:15], v[24:27], v[100:103], a[0:15]
	ds_read_b128 v[24:27], v98 offset:5120
	v_mfma_f32_32x32x16_f16 a[80:95], v[28:31], v[104:107], a[80:95]
	s_add_u32 m0, s46, 0xd3c0
	s_add_u32 s40, s40, 0x1800
	s_addc_u32 s41, s41, 0
	global_load_lds_dwordx4 v76, s[40:41]
	ds_read_b128 v[28:31], v98 offset:6144
	v_mfma_f32_32x32x16_f16 a[64:79], v[32:35], v[104:107], a[64:79]
	ds_read_b128 v[32:35], v98 offset:7168
	v_mfma_f32_32x32x16_f16 a[48:63], v[36:39], v[104:107], a[48:63]
	s_add_u32 m0, s47, 0xd3c0
	s_add_u32 s42, s42, 0x1800
	s_addc_u32 s43, s43, 0
	global_load_lds_dwordx4 v77, s[42:43]
	ds_read_b128 v[36:39], v98 offset:8192
	v_mfma_f32_32x32x16_f16 a[32:47], v[40:43], v[104:107], a[32:47]
	ds_read_b128 v[40:43], v98 offset:9216
	v_mfma_f32_32x32x16_f16 a[16:31], v[44:47], v[104:107], a[16:31]
	s_add_u32 m0, s48, 0xd3c0
	s_add_u32 s44, s44, 0x1800
	s_addc_u32 s45, s45, 0
	global_load_lds_dwordx4 v78, s[44:45]
	ds_read_b128 v[44:47], v98 offset:10240
	v_mfma_f32_32x32x16_f16 a[0:15], v[48:51], v[104:107], a[0:15]
	ds_read_b128 v[48:51], v98 offset:11264
	s_waitcnt lgkmcnt(6)
	v_mfma_f32_32x32x16_f16 a[80:95], v[4:7], v[108:111], a[80:95]
	s_waitcnt vmcnt(24)
	ds_write_b128 v81, v[116:119]
	ds_write_b128 v81, v[120:123] offset:1024
	v_mfma_f32_32x32x16_f16 a[64:79], v[8:11], v[108:111], a[64:79]
	ds_write_b128 v81, v[124:127] offset:2048
	ds_write_b128 v81, v[128:131] offset:3072
	v_mfma_f32_32x32x16_f16 a[48:63], v[12:15], v[108:111], a[48:63]
	ds_read_b128 v[52:55], v95
	ds_read_b128 v[56:59], v96
	ds_read_b128 v[60:63], v97
	ds_read_b128 v[0:3], v94
	s_waitcnt vmcnt(10)
	s_waitcnt lgkmcnt(8)
	s_barrier
	ds_read_b128 v[4:7], v84 offset:0
	ds_read_b128 v[8:11], v84 offset:1024
	ds_read_b128 v[12:15], v84 offset:2048
	v_mfma_f32_32x32x16_f16 a[32:47], v[16:19], v[108:111], a[32:47]
	ds_read_b128 v[16:19], v84 offset:3072
	v_mfma_f32_32x32x16_f16 a[16:31], v[20:23], v[108:111], a[16:31]
	ds_read_b128 v[20:23], v84 offset:4096
	v_mfma_f32_32x32x16_f16 a[0:15], v[24:27], v[108:111], a[0:15]
	ds_read_b128 v[24:27], v84 offset:5120
	s_waitcnt lgkmcnt(6)
	v_mfma_f32_32x32x16_f16 a[80:95], v[28:31], v[112:115], a[80:95]
	s_add_u32 m0, s46, 0x103c0
	s_add_u32 s40, s40, 0x1800
	s_addc_u32 s41, s41, 0
	global_load_lds_dwordx4 v76, s[40:41]
	ds_read_b128 v[28:31], v84 offset:6144
	v_mfma_f32_32x32x16_f16 a[64:79], v[32:35], v[112:115], a[64:79]
	global_load_dwordx4 v[116:119], v64, s[4:5] offset:1152
	global_load_dwordx4 v[120:123], v66, s[4:5] offset:1152
	ds_read_b128 v[32:35], v84 offset:7168
	v_mfma_f32_32x32x16_f16 a[48:63], v[36:39], v[112:115], a[48:63]
	s_add_u32 m0, s47, 0x103c0
	s_add_u32 s42, s42, 0x1800
	s_addc_u32 s43, s43, 0
	global_load_lds_dwordx4 v77, s[42:43]
	ds_read_b128 v[36:39], v84 offset:8192
	v_mfma_f32_32x32x16_f16 a[32:47], v[40:43], v[112:115], a[32:47]
	global_load_dwordx4 v[124:127], v68, s[4:5] offset:1152
	global_load_dwordx4 v[128:131], v70, s[4:5] offset:1152
	ds_read_b128 v[40:43], v84 offset:9216
	v_mfma_f32_32x32x16_f16 a[16:31], v[44:47], v[112:115], a[16:31]
	s_add_u32 m0, s48, 0x103c0
	s_add_u32 s44, s44, 0x1800
	s_addc_u32 s45, s45, 0
	global_load_lds_dwordx4 v78, s[44:45]
	ds_read_b128 v[44:47], v84 offset:10240
	v_mfma_f32_32x32x16_f16 a[0:15], v[48:51], v[112:115], a[0:15]
	ds_read_b128 v[48:51], v84 offset:11264
	s_waitcnt lgkmcnt(6)
	v_mfma_f32_32x32x16_f16 a[80:95], v[4:7], v[52:55], a[80:95]
	v_mfma_f32_32x32x16_f16 a[64:79], v[8:11], v[52:55], a[64:79]
	v_mfma_f32_32x32x16_f16 a[48:63], v[12:15], v[52:55], a[48:63]
	s_waitcnt vmcnt(10)
	s_waitcnt lgkmcnt(0)
	s_barrier
	ds_read_b128 v[4:7], v84 offset:12288
	ds_read_b128 v[8:11], v84 offset:13312
	ds_read_b128 v[12:15], v84 offset:14336
	v_mfma_f32_32x32x16_f16 a[32:47], v[16:19], v[52:55], a[32:47]
	ds_read_b128 v[16:19], v84 offset:15360
	v_mfma_f32_32x32x16_f16 a[16:31], v[20:23], v[52:55], a[16:31]
	ds_read_b128 v[20:23], v84 offset:16384
	v_mfma_f32_32x32x16_f16 a[0:15], v[24:27], v[52:55], a[0:15]
	ds_read_b128 v[24:27], v84 offset:17408
	v_mfma_f32_32x32x16_f16 a[80:95], v[28:31], v[56:59], a[80:95]
	s_add_u32 m0, s46, 0x0
	s_add_u32 s40, s40, 0x1800
	s_addc_u32 s41, s41, 0
	global_load_lds_dwordx4 v76, s[40:41]
	ds_read_b128 v[28:31], v84 offset:18432
	v_mfma_f32_32x32x16_f16 a[64:79], v[32:35], v[56:59], a[64:79]
	ds_read_b128 v[32:35], v84 offset:19456
	v_mfma_f32_32x32x16_f16 a[48:63], v[36:39], v[56:59], a[48:63]
	s_add_u32 m0, s47, 0x0
	s_add_u32 s42, s42, 0x1800
	s_addc_u32 s43, s43, 0
	global_load_lds_dwordx4 v77, s[42:43]
	ds_read_b128 v[36:39], v84 offset:20480
	v_mfma_f32_32x32x16_f16 a[32:47], v[40:43], v[56:59], a[32:47]
	ds_read_b128 v[40:43], v84 offset:21504
	v_mfma_f32_32x32x16_f16 a[16:31], v[44:47], v[56:59], a[16:31]
	s_add_u32 m0, s48, 0x0
	s_add_u32 s44, s44, 0x1800
	s_addc_u32 s45, s45, 0
	global_load_lds_dwordx4 v78, s[44:45]
	ds_read_b128 v[44:47], v84 offset:22528
	v_mfma_f32_32x32x16_f16 a[0:15], v[48:51], v[56:59], a[0:15]
	ds_read_b128 v[48:51], v84 offset:23552
	s_waitcnt lgkmcnt(6)
	v_mfma_f32_32x32x16_f16 a[80:95], v[4:7], v[60:63], a[80:95]
	s_waitcnt vmcnt(24)
	ds_write_b128 v81, v[132:135]
	ds_write_b128 v81, v[136:139] offset:1024
	v_mfma_f32_32x32x16_f16 a[64:79], v[8:11], v[60:63], a[64:79]
	ds_write_b128 v81, v[140:143] offset:2048
	ds_write_b128 v81, v[144:147] offset:3072
	v_mfma_f32_32x32x16_f16 a[48:63], v[12:15], v[60:63], a[48:63]
	ds_read_b128 v[100:103], v95
	ds_read_b128 v[104:107], v96
	ds_read_b128 v[108:111], v97
	ds_read_b128 v[112:115], v94
	s_waitcnt vmcnt(10)
	s_waitcnt lgkmcnt(8)
	s_barrier
	ds_read_b128 v[4:7], v84 offset:54208
	ds_read_b128 v[8:11], v84 offset:55232
	ds_read_b128 v[12:15], v84 offset:56256
	v_mfma_f32_32x32x16_f16 a[32:47], v[16:19], v[60:63], a[32:47]
	ds_read_b128 v[16:19], v84 offset:57280
	v_mfma_f32_32x32x16_f16 a[16:31], v[20:23], v[60:63], a[16:31]
	ds_read_b128 v[20:23], v84 offset:58304
	v_mfma_f32_32x32x16_f16 a[0:15], v[24:27], v[60:63], a[0:15]
	ds_read_b128 v[24:27], v84 offset:59328
	s_waitcnt lgkmcnt(6)
	v_mfma_f32_32x32x16_f16 a[80:95], v[28:31], v[0:3], a[80:95]
	s_add_u32 m0, s46, 0x3000
	s_add_u32 s40, s40, 0x1800
	s_addc_u32 s41, s41, 0
	global_load_lds_dwordx4 v76, s[40:41]
	ds_read_b128 v[28:31], v84 offset:60352
	v_mfma_f32_32x32x16_f16 a[64:79], v[32:35], v[0:3], a[64:79]
	global_load_dwordx4 v[132:135], v64, s[4:5] offset:1280
	global_load_dwordx4 v[136:139], v66, s[4:5] offset:1280
	ds_read_b128 v[32:35], v84 offset:61376
	v_mfma_f32_32x32x16_f16 a[48:63], v[36:39], v[0:3], a[48:63]
	s_add_u32 m0, s47, 0x3000
	s_add_u32 s42, s42, 0x1800
	s_addc_u32 s43, s43, 0
	global_load_lds_dwordx4 v77, s[42:43]
	ds_read_b128 v[36:39], v84 offset:62400
	v_mfma_f32_32x32x16_f16 a[32:47], v[40:43], v[0:3], a[32:47]
	global_load_dwordx4 v[140:143], v68, s[4:5] offset:1280
	global_load_dwordx4 v[144:147], v70, s[4:5] offset:1280
	ds_read_b128 v[40:43], v84 offset:63424
	v_mfma_f32_32x32x16_f16 a[16:31], v[44:47], v[0:3], a[16:31]
	s_add_u32 m0, s48, 0x3000
	s_add_u32 s44, s44, 0x1800
	s_addc_u32 s45, s45, 0
	global_load_lds_dwordx4 v78, s[44:45]
	ds_read_b128 v[44:47], v84 offset:64448
	v_mfma_f32_32x32x16_f16 a[0:15], v[48:51], v[0:3], a[0:15]
	ds_read_b128 v[48:51], v84 offset:65472
	s_waitcnt lgkmcnt(6)
	v_mfma_f32_32x32x16_f16 a[80:95], v[4:7], v[100:103], a[80:95]
	v_mfma_f32_32x32x16_f16 a[64:79], v[8:11], v[100:103], a[64:79]
	v_mfma_f32_32x32x16_f16 a[48:63], v[12:15], v[100:103], a[48:63]
	s_waitcnt vmcnt(10)
	s_waitcnt lgkmcnt(0)
	s_barrier
	ds_read_b128 v[4:7], v98
	ds_read_b128 v[8:11], v98 offset:1024
	ds_read_b128 v[12:15], v98 offset:2048
	v_mfma_f32_32x32x16_f16 a[32:47], v[16:19], v[100:103], a[32:47]
	ds_read_b128 v[16:19], v98 offset:3072
	v_mfma_f32_32x32x16_f16 a[16:31], v[20:23], v[100:103], a[16:31]
	ds_read_b128 v[20:23], v98 offset:4096
	v_mfma_f32_32x32x16_f16 a[0:15], v[24:27], v[100:103], a[0:15]
	ds_read_b128 v[24:27], v98 offset:5120
	v_mfma_f32_32x32x16_f16 a[80:95], v[28:31], v[104:107], a[80:95]
	s_add_u32 m0, s46, 0xd3c0
	s_add_u32 s40, s40, 0x1800
	s_addc_u32 s41, s41, 0
	global_load_lds_dwordx4 v76, s[40:41]
	ds_read_b128 v[28:31], v98 offset:6144
	v_mfma_f32_32x32x16_f16 a[64:79], v[32:35], v[104:107], a[64:79]
	ds_read_b128 v[32:35], v98 offset:7168
	v_mfma_f32_32x32x16_f16 a[48:63], v[36:39], v[104:107], a[48:63]
	s_add_u32 m0, s47, 0xd3c0
	s_add_u32 s42, s42, 0x1800
	s_addc_u32 s43, s43, 0
	global_load_lds_dwordx4 v77, s[42:43]
	ds_read_b128 v[36:39], v98 offset:8192
	v_mfma_f32_32x32x16_f16 a[32:47], v[40:43], v[104:107], a[32:47]
	ds_read_b128 v[40:43], v98 offset:9216
	v_mfma_f32_32x32x16_f16 a[16:31], v[44:47], v[104:107], a[16:31]
	s_add_u32 m0, s48, 0xd3c0
	s_add_u32 s44, s44, 0x1800
	s_addc_u32 s45, s45, 0
	global_load_lds_dwordx4 v78, s[44:45]
	ds_read_b128 v[44:47], v98 offset:10240
	v_mfma_f32_32x32x16_f16 a[0:15], v[48:51], v[104:107], a[0:15]
	ds_read_b128 v[48:51], v98 offset:11264
	s_waitcnt lgkmcnt(6)
	v_mfma_f32_32x32x16_f16 a[80:95], v[4:7], v[108:111], a[80:95]
	s_waitcnt vmcnt(24)
	ds_write_b128 v81, v[148:151]
	ds_write_b128 v81, v[152:155] offset:1024
	v_mfma_f32_32x32x16_f16 a[64:79], v[8:11], v[108:111], a[64:79]
	ds_write_b128 v81, v[156:159] offset:2048
	ds_write_b128 v81, v[72:75] offset:3072
	v_mfma_f32_32x32x16_f16 a[48:63], v[12:15], v[108:111], a[48:63]
	ds_read_b128 v[52:55], v95
	ds_read_b128 v[56:59], v96
	ds_read_b128 v[60:63], v97
	ds_read_b128 v[0:3], v94
	s_waitcnt vmcnt(10)
	s_waitcnt lgkmcnt(8)
	s_barrier
	ds_read_b128 v[4:7], v84 offset:0
	ds_read_b128 v[8:11], v84 offset:1024
	ds_read_b128 v[12:15], v84 offset:2048
	v_mfma_f32_32x32x16_f16 a[32:47], v[16:19], v[108:111], a[32:47]
	ds_read_b128 v[16:19], v84 offset:3072
	v_mfma_f32_32x32x16_f16 a[16:31], v[20:23], v[108:111], a[16:31]
	ds_read_b128 v[20:23], v84 offset:4096
	v_mfma_f32_32x32x16_f16 a[0:15], v[24:27], v[108:111], a[0:15]
	ds_read_b128 v[24:27], v84 offset:5120
	s_waitcnt lgkmcnt(6)
	v_mfma_f32_32x32x16_f16 a[80:95], v[28:31], v[112:115], a[80:95]
	s_add_u32 m0, s46, 0x103c0
	s_add_u32 s40, s40, 0x1800
	s_addc_u32 s41, s41, 0
	global_load_lds_dwordx4 v76, s[40:41]
	ds_read_b128 v[28:31], v84 offset:6144
	v_mfma_f32_32x32x16_f16 a[64:79], v[32:35], v[112:115], a[64:79]
	global_load_dwordx4 v[148:151], v64, s[4:5] offset:1408
	global_load_dwordx4 v[152:155], v66, s[4:5] offset:1408
	ds_read_b128 v[32:35], v84 offset:7168
	v_mfma_f32_32x32x16_f16 a[48:63], v[36:39], v[112:115], a[48:63]
	s_add_u32 m0, s47, 0x103c0
	s_add_u32 s42, s42, 0x1800
	s_addc_u32 s43, s43, 0
	global_load_lds_dwordx4 v77, s[42:43]
	ds_read_b128 v[36:39], v84 offset:8192
	v_mfma_f32_32x32x16_f16 a[32:47], v[40:43], v[112:115], a[32:47]
	global_load_dwordx4 v[156:159], v68, s[4:5] offset:1408
	global_load_dwordx4 v[72:75], v70, s[4:5] offset:1408
	ds_read_b128 v[40:43], v84 offset:9216
	v_mfma_f32_32x32x16_f16 a[16:31], v[44:47], v[112:115], a[16:31]
	s_add_u32 m0, s48, 0x103c0
	s_add_u32 s44, s44, 0x1800
	s_addc_u32 s45, s45, 0
	global_load_lds_dwordx4 v78, s[44:45]
	ds_read_b128 v[44:47], v84 offset:10240
	v_mfma_f32_32x32x16_f16 a[0:15], v[48:51], v[112:115], a[0:15]
	ds_read_b128 v[48:51], v84 offset:11264
	s_waitcnt lgkmcnt(6)
	v_mfma_f32_32x32x16_f16 a[80:95], v[4:7], v[52:55], a[80:95]
	v_mfma_f32_32x32x16_f16 a[64:79], v[8:11], v[52:55], a[64:79]
	v_mfma_f32_32x32x16_f16 a[48:63], v[12:15], v[52:55], a[48:63]
	s_waitcnt vmcnt(10)
	s_waitcnt lgkmcnt(0)
	s_barrier
	ds_read_b128 v[4:7], v84 offset:12288
	ds_read_b128 v[8:11], v84 offset:13312
	ds_read_b128 v[12:15], v84 offset:14336
	v_mfma_f32_32x32x16_f16 a[32:47], v[16:19], v[52:55], a[32:47]
	ds_read_b128 v[16:19], v84 offset:15360
	v_mfma_f32_32x32x16_f16 a[16:31], v[20:23], v[52:55], a[16:31]
	ds_read_b128 v[20:23], v84 offset:16384
	v_mfma_f32_32x32x16_f16 a[0:15], v[24:27], v[52:55], a[0:15]
	ds_read_b128 v[24:27], v84 offset:17408
	v_mfma_f32_32x32x16_f16 a[80:95], v[28:31], v[56:59], a[80:95]
	s_add_u32 m0, s46, 0x0
	s_add_u32 s40, s40, 0x1800
	s_addc_u32 s41, s41, 0
	global_load_lds_dwordx4 v76, s[40:41]
	ds_read_b128 v[28:31], v84 offset:18432
	v_mfma_f32_32x32x16_f16 a[64:79], v[32:35], v[56:59], a[64:79]
	ds_read_b128 v[32:35], v84 offset:19456
	v_mfma_f32_32x32x16_f16 a[48:63], v[36:39], v[56:59], a[48:63]
	s_add_u32 m0, s47, 0x0
	s_add_u32 s42, s42, 0x1800
	s_addc_u32 s43, s43, 0
	global_load_lds_dwordx4 v77, s[42:43]
	ds_read_b128 v[36:39], v84 offset:20480
	v_mfma_f32_32x32x16_f16 a[32:47], v[40:43], v[56:59], a[32:47]
	ds_read_b128 v[40:43], v84 offset:21504
	v_mfma_f32_32x32x16_f16 a[16:31], v[44:47], v[56:59], a[16:31]
	s_add_u32 m0, s48, 0x0
	s_add_u32 s44, s44, 0x1800
	s_addc_u32 s45, s45, 0
	global_load_lds_dwordx4 v78, s[44:45]
	ds_read_b128 v[44:47], v84 offset:22528
	v_mfma_f32_32x32x16_f16 a[0:15], v[48:51], v[56:59], a[0:15]
	ds_read_b128 v[48:51], v84 offset:23552
	s_waitcnt lgkmcnt(6)
	v_mfma_f32_32x32x16_f16 a[80:95], v[4:7], v[60:63], a[80:95]
	s_waitcnt vmcnt(24)
	ds_write_b128 v81, v[116:119]
	ds_write_b128 v81, v[120:123] offset:1024
	v_mfma_f32_32x32x16_f16 a[64:79], v[8:11], v[60:63], a[64:79]
	ds_write_b128 v81, v[124:127] offset:2048
	ds_write_b128 v81, v[128:131] offset:3072
	v_mfma_f32_32x32x16_f16 a[48:63], v[12:15], v[60:63], a[48:63]
	ds_read_b128 v[100:103], v95
	ds_read_b128 v[104:107], v96
	ds_read_b128 v[108:111], v97
	ds_read_b128 v[112:115], v94
	s_waitcnt vmcnt(10)
	s_waitcnt lgkmcnt(8)
	s_barrier
	ds_read_b128 v[4:7], v84 offset:54208
	ds_read_b128 v[8:11], v84 offset:55232
	ds_read_b128 v[12:15], v84 offset:56256
	v_mfma_f32_32x32x16_f16 a[32:47], v[16:19], v[60:63], a[32:47]
	ds_read_b128 v[16:19], v84 offset:57280
	v_mfma_f32_32x32x16_f16 a[16:31], v[20:23], v[60:63], a[16:31]
	ds_read_b128 v[20:23], v84 offset:58304
	v_mfma_f32_32x32x16_f16 a[0:15], v[24:27], v[60:63], a[0:15]
	ds_read_b128 v[24:27], v84 offset:59328
	s_waitcnt lgkmcnt(6)
	v_mfma_f32_32x32x16_f16 a[80:95], v[28:31], v[0:3], a[80:95]
	s_add_u32 m0, s46, 0x3000
	s_add_u32 s40, s40, 0x1800
	s_addc_u32 s41, s41, 0
	global_load_lds_dwordx4 v76, s[40:41]
	ds_read_b128 v[28:31], v84 offset:60352
	v_mfma_f32_32x32x16_f16 a[64:79], v[32:35], v[0:3], a[64:79]
	global_load_dwordx4 v[116:119], v64, s[4:5] offset:1440
	global_load_dwordx4 v[120:123], v66, s[4:5] offset:1440
	ds_read_b128 v[32:35], v84 offset:61376
	v_mfma_f32_32x32x16_f16 a[48:63], v[36:39], v[0:3], a[48:63]
	s_add_u32 m0, s47, 0x3000
	s_add_u32 s42, s42, 0x1800
	s_addc_u32 s43, s43, 0
	global_load_lds_dwordx4 v77, s[42:43]
	ds_read_b128 v[36:39], v84 offset:62400
	v_mfma_f32_32x32x16_f16 a[32:47], v[40:43], v[0:3], a[32:47]
	global_load_dwordx4 v[124:127], v68, s[4:5] offset:1440
	global_load_dwordx4 v[128:131], v70, s[4:5] offset:1440
	ds_read_b128 v[40:43], v84 offset:63424
	v_mfma_f32_32x32x16_f16 a[16:31], v[44:47], v[0:3], a[16:31]
	s_add_u32 m0, s48, 0x3000
	s_add_u32 s44, s44, 0x1800
	s_addc_u32 s45, s45, 0
	global_load_lds_dwordx4 v78, s[44:45]
	ds_read_b128 v[44:47], v84 offset:64448
	v_mfma_f32_32x32x16_f16 a[0:15], v[48:51], v[0:3], a[0:15]
	ds_read_b128 v[48:51], v84 offset:65472
	s_waitcnt lgkmcnt(6)
	v_mfma_f32_32x32x16_f16 a[80:95], v[4:7], v[100:103], a[80:95]
	v_mfma_f32_32x32x16_f16 a[64:79], v[8:11], v[100:103], a[64:79]
	v_mfma_f32_32x32x16_f16 a[48:63], v[12:15], v[100:103], a[48:63]
	s_waitcnt vmcnt(10)
	s_waitcnt lgkmcnt(0)
	s_barrier
	ds_read_b128 v[4:7], v98
	ds_read_b128 v[8:11], v98 offset:1024
	ds_read_b128 v[12:15], v98 offset:2048
	v_mfma_f32_32x32x16_f16 a[32:47], v[16:19], v[100:103], a[32:47]
	ds_read_b128 v[16:19], v98 offset:3072
	v_mfma_f32_32x32x16_f16 a[16:31], v[20:23], v[100:103], a[16:31]
	ds_read_b128 v[20:23], v98 offset:4096
	v_mfma_f32_32x32x16_f16 a[0:15], v[24:27], v[100:103], a[0:15]
	ds_read_b128 v[24:27], v98 offset:5120
	v_mfma_f32_32x32x16_f16 a[80:95], v[28:31], v[104:107], a[80:95]
	s_add_u32 m0, s46, 0xd3c0
	s_add_u32 s40, s40, 0x1800
	s_addc_u32 s41, s41, 0
	global_load_lds_dwordx4 v76, s[40:41]
	ds_read_b128 v[28:31], v98 offset:6144
	v_mfma_f32_32x32x16_f16 a[64:79], v[32:35], v[104:107], a[64:79]
	ds_read_b128 v[32:35], v98 offset:7168
	v_mfma_f32_32x32x16_f16 a[48:63], v[36:39], v[104:107], a[48:63]
	s_add_u32 m0, s47, 0xd3c0
	s_add_u32 s42, s42, 0x1800
	s_addc_u32 s43, s43, 0
	global_load_lds_dwordx4 v77, s[42:43]
	ds_read_b128 v[36:39], v98 offset:8192
	v_mfma_f32_32x32x16_f16 a[32:47], v[40:43], v[104:107], a[32:47]
	ds_read_b128 v[40:43], v98 offset:9216
	v_mfma_f32_32x32x16_f16 a[16:31], v[44:47], v[104:107], a[16:31]
	s_add_u32 m0, s48, 0xd3c0
	s_add_u32 s44, s44, 0x1800
	s_addc_u32 s45, s45, 0
	global_load_lds_dwordx4 v78, s[44:45]
	ds_read_b128 v[44:47], v98 offset:10240
	v_mfma_f32_32x32x16_f16 a[0:15], v[48:51], v[104:107], a[0:15]
	ds_read_b128 v[48:51], v98 offset:11264
	s_waitcnt lgkmcnt(6)
	v_mfma_f32_32x32x16_f16 a[80:95], v[4:7], v[108:111], a[80:95]
	s_waitcnt vmcnt(24)
	ds_write_b128 v81, v[132:135]
	ds_write_b128 v81, v[136:139] offset:1024
	v_mfma_f32_32x32x16_f16 a[64:79], v[8:11], v[108:111], a[64:79]
	ds_write_b128 v81, v[140:143] offset:2048
	ds_write_b128 v81, v[144:147] offset:3072
	v_mfma_f32_32x32x16_f16 a[48:63], v[12:15], v[108:111], a[48:63]
	ds_read_b128 v[52:55], v95
	ds_read_b128 v[56:59], v96
	ds_read_b128 v[60:63], v97
	ds_read_b128 v[0:3], v94
	s_waitcnt vmcnt(10)
	s_waitcnt lgkmcnt(8)
	s_barrier
	ds_read_b128 v[4:7], v84 offset:0
	ds_read_b128 v[8:11], v84 offset:1024
	ds_read_b128 v[12:15], v84 offset:2048
	v_mfma_f32_32x32x16_f16 a[32:47], v[16:19], v[108:111], a[32:47]
	ds_read_b128 v[16:19], v84 offset:3072
	v_mfma_f32_32x32x16_f16 a[16:31], v[20:23], v[108:111], a[16:31]
	ds_read_b128 v[20:23], v84 offset:4096
	v_mfma_f32_32x32x16_f16 a[0:15], v[24:27], v[108:111], a[0:15]
	ds_read_b128 v[24:27], v84 offset:5120
	s_waitcnt lgkmcnt(6)
	v_mfma_f32_32x32x16_f16 a[80:95], v[28:31], v[112:115], a[80:95]
	s_add_u32 m0, s46, 0x103c0
	s_add_u32 s40, s40, 0x1800
	s_addc_u32 s41, s41, 0
	global_load_lds_dwordx4 v76, s[40:41]
	ds_read_b128 v[28:31], v84 offset:6144
	v_mfma_f32_32x32x16_f16 a[64:79], v[32:35], v[112:115], a[64:79]
	ds_read_b128 v[32:35], v84 offset:7168
	v_mfma_f32_32x32x16_f16 a[48:63], v[36:39], v[112:115], a[48:63]
	s_add_u32 m0, s47, 0x103c0
	s_add_u32 s42, s42, 0x1800
	s_addc_u32 s43, s43, 0
	global_load_lds_dwordx4 v77, s[42:43]
	ds_read_b128 v[36:39], v84 offset:8192
	v_mfma_f32_32x32x16_f16 a[32:47], v[40:43], v[112:115], a[32:47]
	ds_read_b128 v[40:43], v84 offset:9216
	v_mfma_f32_32x32x16_f16 a[16:31], v[44:47], v[112:115], a[16:31]
	s_add_u32 m0, s48, 0x103c0
	s_add_u32 s44, s44, 0x1800
	s_addc_u32 s45, s45, 0
	global_load_lds_dwordx4 v78, s[44:45]
	ds_read_b128 v[44:47], v84 offset:10240
	v_mfma_f32_32x32x16_f16 a[0:15], v[48:51], v[112:115], a[0:15]
	ds_read_b128 v[48:51], v84 offset:11264
	s_waitcnt lgkmcnt(6)
	v_mfma_f32_32x32x16_f16 a[80:95], v[4:7], v[52:55], a[80:95]
	v_mfma_f32_32x32x16_f16 a[64:79], v[8:11], v[52:55], a[64:79]
	v_mfma_f32_32x32x16_f16 a[48:63], v[12:15], v[52:55], a[48:63]
	s_waitcnt vmcnt(6)
	s_waitcnt lgkmcnt(0)
	s_barrier
	ds_read_b128 v[4:7], v84 offset:12288
	ds_read_b128 v[8:11], v84 offset:13312
	ds_read_b128 v[12:15], v84 offset:14336
	v_mfma_f32_32x32x16_f16 a[32:47], v[16:19], v[52:55], a[32:47]
	ds_read_b128 v[16:19], v84 offset:15360
	v_mfma_f32_32x32x16_f16 a[16:31], v[20:23], v[52:55], a[16:31]
	ds_read_b128 v[20:23], v84 offset:16384
	v_mfma_f32_32x32x16_f16 a[0:15], v[24:27], v[52:55], a[0:15]
	ds_read_b128 v[24:27], v84 offset:17408
	v_mfma_f32_32x32x16_f16 a[80:95], v[28:31], v[56:59], a[80:95]
	s_add_u32 m0, s46, 0x0
	s_add_u32 s40, s40, 0x1800
	s_addc_u32 s41, s41, 0
	global_load_lds_dwordx4 v76, s[40:41]
	ds_read_b128 v[28:31], v84 offset:18432
	v_mfma_f32_32x32x16_f16 a[64:79], v[32:35], v[56:59], a[64:79]
	ds_read_b128 v[32:35], v84 offset:19456
	v_mfma_f32_32x32x16_f16 a[48:63], v[36:39], v[56:59], a[48:63]
	s_add_u32 m0, s47, 0x0
	s_add_u32 s42, s42, s49
	s_addc_u32 s43, s43, 0
	global_load_lds_dwordx4 v77, s[42:43]
	ds_read_b128 v[36:39], v84 offset:20480
	v_mfma_f32_32x32x16_f16 a[32:47], v[40:43], v[56:59], a[32:47]
	ds_read_b128 v[40:43], v84 offset:21504
	v_mfma_f32_32x32x16_f16 a[16:31], v[44:47], v[56:59], a[16:31]
	s_add_u32 m0, s48, 0x0
	s_add_u32 s44, s44, 0xc00
	s_addc_u32 s45, s45, 0
	global_load_lds_dwordx4 v78, s[44:45]
	ds_read_b128 v[44:47], v84 offset:22528
	v_mfma_f32_32x32x16_f16 a[0:15], v[48:51], v[56:59], a[0:15]
	ds_read_b128 v[48:51], v84 offset:23552
	s_waitcnt lgkmcnt(6)
	v_mfma_f32_32x32x16_f16 a[80:95], v[4:7], v[60:63], a[80:95]
	s_waitcnt vmcnt(20)
	ds_write_b128 v81, v[148:151]
	ds_write_b128 v81, v[152:155] offset:1024
	v_mfma_f32_32x32x16_f16 a[64:79], v[8:11], v[60:63], a[64:79]
	ds_write_b128 v81, v[156:159] offset:2048
	ds_write_b128 v81, v[72:75] offset:3072
	v_mfma_f32_32x32x16_f16 a[48:63], v[12:15], v[60:63], a[48:63]
	ds_read_b128 v[100:103], v95
	ds_read_b128 v[104:107], v96
	ds_read_b128 v[108:111], v97
	ds_read_b128 v[112:115], v94
	s_waitcnt vmcnt(6)
	s_waitcnt lgkmcnt(8)
	s_barrier
	ds_read_b128 v[4:7], v84 offset:54208
	ds_read_b128 v[8:11], v84 offset:55232
	ds_read_b128 v[12:15], v84 offset:56256
	v_mfma_f32_32x32x16_f16 a[32:47], v[16:19], v[60:63], a[32:47]
	ds_read_b128 v[16:19], v84 offset:57280
	v_mfma_f32_32x32x16_f16 a[16:31], v[20:23], v[60:63], a[16:31]
	ds_read_b128 v[20:23], v84 offset:58304
	v_mfma_f32_32x32x16_f16 a[0:15], v[24:27], v[60:63], a[0:15]
	ds_read_b128 v[24:27], v84 offset:59328
	s_waitcnt lgkmcnt(6)
	v_mfma_f32_32x32x16_f16 a[80:95], v[28:31], v[0:3], a[80:95]
	ds_read_b128 v[28:31], v84 offset:60352
	v_mfma_f32_32x32x16_f16 a[64:79], v[32:35], v[0:3], a[64:79]
	ds_read_b128 v[32:35], v84 offset:61376
	v_mfma_f32_32x32x16_f16 a[48:63], v[36:39], v[0:3], a[48:63]
	ds_read_b128 v[36:39], v84 offset:62400
	v_mfma_f32_32x32x16_f16 a[32:47], v[40:43], v[0:3], a[32:47]
	ds_read_b128 v[40:43], v84 offset:63424
	v_mfma_f32_32x32x16_f16 a[16:31], v[44:47], v[0:3], a[16:31]
	ds_read_b128 v[44:47], v84 offset:64448
	v_mfma_f32_32x32x16_f16 a[0:15], v[48:51], v[0:3], a[0:15]
	ds_read_b128 v[48:51], v84 offset:65472
	s_waitcnt lgkmcnt(6)
	v_mfma_f32_32x32x16_f16 a[80:95], v[4:7], v[100:103], a[80:95]
	v_mfma_f32_32x32x16_f16 a[64:79], v[8:11], v[100:103], a[64:79]
	v_mfma_f32_32x32x16_f16 a[48:63], v[12:15], v[100:103], a[48:63]
	s_waitcnt vmcnt(3)
	s_waitcnt lgkmcnt(0)
	s_barrier
	ds_read_b128 v[4:7], v98
	ds_read_b128 v[8:11], v98 offset:1024
	ds_read_b128 v[12:15], v98 offset:2048
	v_mfma_f32_32x32x16_f16 a[32:47], v[16:19], v[100:103], a[32:47]
	ds_read_b128 v[16:19], v98 offset:3072
	v_mfma_f32_32x32x16_f16 a[16:31], v[20:23], v[100:103], a[16:31]
	ds_read_b128 v[20:23], v98 offset:4096
	v_mfma_f32_32x32x16_f16 a[0:15], v[24:27], v[100:103], a[0:15]
	ds_read_b128 v[24:27], v98 offset:5120
	v_mfma_f32_32x32x16_f16 a[80:95], v[28:31], v[104:107], a[80:95]
	ds_read_b128 v[28:31], v98 offset:6144
	v_mfma_f32_32x32x16_f16 a[64:79], v[32:35], v[104:107], a[64:79]
	ds_read_b128 v[32:35], v98 offset:7168
	v_mfma_f32_32x32x16_f16 a[48:63], v[36:39], v[104:107], a[48:63]
	ds_read_b128 v[36:39], v98 offset:8192
	v_mfma_f32_32x32x16_f16 a[32:47], v[40:43], v[104:107], a[32:47]
	ds_read_b128 v[40:43], v98 offset:9216
	v_mfma_f32_32x32x16_f16 a[16:31], v[44:47], v[104:107], a[16:31]
	ds_read_b128 v[44:47], v98 offset:10240
	v_mfma_f32_32x32x16_f16 a[0:15], v[48:51], v[104:107], a[0:15]
	ds_read_b128 v[48:51], v98 offset:11264
	s_waitcnt lgkmcnt(6)
	v_mfma_f32_32x32x16_f16 a[80:95], v[4:7], v[108:111], a[80:95]
	s_waitcnt vmcnt(10)
	ds_write_b128 v81, v[116:119]
	ds_write_b128 v81, v[120:123] offset:1024
	v_mfma_f32_32x32x16_f16 a[64:79], v[8:11], v[108:111], a[64:79]
	ds_write_b128 v81, v[124:127] offset:2048
	ds_write_b128 v81, v[128:131] offset:3072
	v_mfma_f32_32x32x16_f16 a[48:63], v[12:15], v[108:111], a[48:63]
	ds_read_b128 v[0:3], v94
	s_waitcnt vmcnt(0)
	s_waitcnt lgkmcnt(5)
	s_barrier
	ds_read_b128 v[4:7], v84 offset:0
	ds_read_b128 v[8:11], v84 offset:1024
	ds_read_b128 v[12:15], v84 offset:2048
	v_mfma_f32_32x32x16_f16 a[32:47], v[16:19], v[108:111], a[32:47]
	ds_read_b128 v[16:19], v84 offset:3072
	v_mfma_f32_32x32x16_f16 a[16:31], v[20:23], v[108:111], a[16:31]
	ds_read_b128 v[20:23], v84 offset:4096
	v_mfma_f32_32x32x16_f16 a[0:15], v[24:27], v[108:111], a[0:15]
	ds_read_b128 v[24:27], v84 offset:5120
	s_waitcnt lgkmcnt(6)
	v_mfma_f32_32x32x16_f16 a[80:95], v[28:31], v[112:115], a[80:95]
	v_mfma_f32_32x32x16_f16 a[64:79], v[32:35], v[112:115], a[64:79]
	v_mfma_f32_32x32x16_f16 a[48:63], v[36:39], v[112:115], a[48:63]
	v_mfma_f32_32x32x16_f16 a[32:47], v[40:43], v[112:115], a[32:47]
	v_mfma_f32_32x32x16_f16 a[16:31], v[44:47], v[112:115], a[16:31]
	v_mfma_f32_32x32x16_f16 a[0:15], v[48:51], v[112:115], a[0:15]
	s_waitcnt lgkmcnt(0)
	v_mfma_f32_32x32x16_f16 a[80:95], v[4:7], v[0:3], a[80:95]
	v_mfma_f32_32x32x16_f16 a[16:31], v[20:23], v[0:3], a[16:31]
	v_lshlrev_b32_e32 v22, 4, v85
	v_mfma_f32_32x32x16_f16 a[64:79], v[8:11], v[0:3], a[64:79]
	v_mfma_f32_32x32x16_f16 a[48:63], v[12:15], v[0:3], a[48:63]
	s_nop 7
	v_accvgpr_read_b32 v13, a88
	v_mfma_f32_32x32x16_f16 a[32:47], v[16:19], v[0:3], a[32:47]
	v_accvgpr_read_b32 v17, a92
	v_mfma_f32_32x32x16_f16 a[0:15], v[24:27], v[0:3], a[0:15]
	ds_read_b128 v[2:5], v22 offset:53248
	ds_read_b128 v[6:9], v22 offset:53280
	v_accvgpr_read_b32 v1, a80
	v_lshlrev_b32_e32 v0, 4, v92
	s_waitcnt lgkmcnt(1)
	v_add_f32_e32 v1, v1, v2
	v_accvgpr_read_b32 v2, a81
	v_add_f32_e32 v2, v3, v2
	v_max_f32_e32 v10, 0, v2
	v_accvgpr_read_b32 v2, a82
	v_add_f32_e32 v2, v4, v2
	v_max_f32_e32 v11, 0, v2
	v_accvgpr_read_b32 v2, a83
	v_add_f32_e32 v2, v5, v2
	v_max_f32_e32 v12, 0, v2
	v_accvgpr_read_b32 v2, a84
	s_waitcnt lgkmcnt(0)
	v_add_f32_e32 v2, v2, v6
	v_max_f32_e32 v6, 0, v2
	v_accvgpr_read_b32 v2, a85
	v_add_f32_e32 v2, v7, v2
	v_max_f32_e32 v7, 0, v2
	v_accvgpr_read_b32 v2, a86
	v_add_f32_e32 v2, v8, v2
	v_max_f32_e32 v8, 0, v2
	v_accvgpr_read_b32 v2, a87
	v_add_f32_e32 v2, v9, v2
	v_max_f32_e32 v9, 0, v2
	ds_read_b128 v[2:5], v22 offset:53312
	v_max_f32_e32 v1, 0, v1
	s_waitcnt lgkmcnt(0)
	v_add_f32_e32 v2, v13, v2
	v_max_f32_e32 v13, 0, v2
	v_accvgpr_read_b32 v2, a89
	v_add_f32_e32 v2, v3, v2
	v_max_f32_e32 v14, 0, v2
	v_accvgpr_read_b32 v2, a90
	v_add_f32_e32 v2, v4, v2
	v_max_f32_e32 v15, 0, v2
	v_accvgpr_read_b32 v2, a91
	v_add_f32_e32 v2, v5, v2
	v_max_f32_e32 v16, 0, v2
	ds_read_b128 v[2:5], v22 offset:53344
	s_waitcnt lgkmcnt(0)
	v_add_f32_e32 v2, v17, v2
	v_max_f32_e32 v17, 0, v2
	v_accvgpr_read_b32 v2, a93
	v_add_f32_e32 v2, v3, v2
	v_max_f32_e32 v18, 0, v2
	v_accvgpr_read_b32 v2, a94
	v_add_f32_e32 v2, v4, v2
	v_max_f32_e32 v19, 0, v2
	v_accvgpr_read_b32 v2, a95
	v_add_f32_e32 v2, v5, v2
	v_cvt_pk_f16_f32 v5, v8, v9
	v_cvt_pk_f16_f32 v4, v6, v7
	ds_read_b128 v[6:9], v0 offset:40960
	v_max_f32_e32 v20, 0, v2
	v_cvt_pk_f16_f32 v3, v11, v12
	v_cvt_pk_f16_f32 v2, v1, v10
	v_accvgpr_read_b32 v1, a64
	s_waitcnt lgkmcnt(0)
	v_mfma_f32_32x32x16_f16 a[80:95], v[6:9], v[2:5], 0
	ds_read_b128 v[6:9], v0 offset:41984
	v_cvt_pk_f16_f32 v5, v19, v20
	v_cvt_pk_f16_f32 v4, v17, v18
	v_cvt_pk_f16_f32 v3, v15, v16
	v_cvt_pk_f16_f32 v2, v13, v14
	v_accvgpr_read_b32 v13, a72
	v_accvgpr_read_b32 v17, a76
	s_waitcnt lgkmcnt(0)
	v_mfma_f32_32x32x16_f16 a[80:95], v[6:9], v[2:5], a[80:95]
	ds_read_b128 v[2:5], v22 offset:53376
	v_accvgpr_read_b32 v9, a68
	s_waitcnt lgkmcnt(0)
	v_add_f32_e32 v1, v1, v2
	v_accvgpr_read_b32 v2, a65
	v_add_f32_e32 v2, v3, v2
	v_max_f32_e32 v6, 0, v2
	v_accvgpr_read_b32 v2, a66
	v_add_f32_e32 v2, v4, v2
	v_max_f32_e32 v7, 0, v2
	v_accvgpr_read_b32 v2, a67
	v_add_f32_e32 v2, v5, v2
	v_max_f32_e32 v8, 0, v2
	ds_read_b128 v[2:5], v22 offset:53408
	v_max_f32_e32 v1, 0, v1
	s_waitcnt lgkmcnt(0)
	v_add_f32_e32 v2, v9, v2
	v_max_f32_e32 v9, 0, v2
	v_accvgpr_read_b32 v2, a69
	v_add_f32_e32 v2, v3, v2
	v_max_f32_e32 v10, 0, v2
	v_accvgpr_read_b32 v2, a70
	v_add_f32_e32 v2, v4, v2
	v_max_f32_e32 v11, 0, v2
	v_accvgpr_read_b32 v2, a71
	v_add_f32_e32 v2, v5, v2
	v_max_f32_e32 v12, 0, v2
	ds_read_b128 v[2:5], v22 offset:53440
	s_waitcnt lgkmcnt(0)
	v_add_f32_e32 v2, v13, v2
	v_max_f32_e32 v13, 0, v2
	v_accvgpr_read_b32 v2, a73
	v_add_f32_e32 v2, v3, v2
	v_max_f32_e32 v14, 0, v2
	v_accvgpr_read_b32 v2, a74
	v_add_f32_e32 v2, v4, v2
	v_max_f32_e32 v15, 0, v2
	v_accvgpr_read_b32 v2, a75
	v_add_f32_e32 v2, v5, v2
	v_max_f32_e32 v16, 0, v2
	ds_read_b128 v[2:5], v22 offset:53472
	s_waitcnt lgkmcnt(0)
	v_add_f32_e32 v2, v17, v2
	v_max_f32_e32 v17, 0, v2
	v_accvgpr_read_b32 v2, a77
	v_add_f32_e32 v2, v3, v2
	v_max_f32_e32 v18, 0, v2
	v_accvgpr_read_b32 v2, a78
	v_add_f32_e32 v2, v4, v2
	v_max_f32_e32 v19, 0, v2
	v_accvgpr_read_b32 v2, a79
	v_add_f32_e32 v2, v5, v2
	v_max_f32_e32 v20, 0, v2
	v_cvt_pk_f16_f32 v4, v9, v10
	v_cvt_pk_f16_f32 v3, v7, v8
	v_cvt_pk_f16_f32 v2, v1, v6
	ds_read_b128 v[6:9], v0 offset:43008
	v_cvt_pk_f16_f32 v5, v11, v12
	v_accvgpr_read_b32 v1, a48
	s_waitcnt lgkmcnt(0)
	v_mfma_f32_32x32x16_f16 a[80:95], v[6:9], v[2:5], a[80:95]
	ds_read_b128 v[6:9], v0 offset:44032
	v_cvt_pk_f16_f32 v5, v19, v20
	v_cvt_pk_f16_f32 v4, v17, v18
	v_cvt_pk_f16_f32 v3, v15, v16
	v_cvt_pk_f16_f32 v2, v13, v14
	v_accvgpr_read_b32 v13, a56
	v_accvgpr_read_b32 v17, a60
	s_waitcnt lgkmcnt(0)
	v_mfma_f32_32x32x16_f16 a[80:95], v[6:9], v[2:5], a[80:95]
	ds_read_b128 v[2:5], v22 offset:53504
	v_accvgpr_read_b32 v9, a52
	s_waitcnt lgkmcnt(0)
	v_add_f32_e32 v1, v1, v2
	v_accvgpr_read_b32 v2, a49
	v_add_f32_e32 v2, v3, v2
	v_max_f32_e32 v6, 0, v2
	v_accvgpr_read_b32 v2, a50
	v_add_f32_e32 v2, v4, v2
	v_max_f32_e32 v7, 0, v2
	v_accvgpr_read_b32 v2, a51
	v_add_f32_e32 v2, v5, v2
	v_max_f32_e32 v8, 0, v2
	ds_read_b128 v[2:5], v22 offset:53536
	v_max_f32_e32 v1, 0, v1
	s_waitcnt lgkmcnt(0)
	v_add_f32_e32 v2, v9, v2
	v_max_f32_e32 v9, 0, v2
	v_accvgpr_read_b32 v2, a53
	v_add_f32_e32 v2, v3, v2
	v_max_f32_e32 v10, 0, v2
	v_accvgpr_read_b32 v2, a54
	v_add_f32_e32 v2, v4, v2
	v_max_f32_e32 v11, 0, v2
	v_accvgpr_read_b32 v2, a55
	v_add_f32_e32 v2, v5, v2
	v_max_f32_e32 v12, 0, v2
	ds_read_b128 v[2:5], v22 offset:53568
	s_waitcnt lgkmcnt(0)
	v_add_f32_e32 v2, v13, v2
	v_max_f32_e32 v13, 0, v2
	v_accvgpr_read_b32 v2, a57
	v_add_f32_e32 v2, v3, v2
	v_max_f32_e32 v14, 0, v2
	v_accvgpr_read_b32 v2, a58
	v_add_f32_e32 v2, v4, v2
	v_max_f32_e32 v15, 0, v2
	v_accvgpr_read_b32 v2, a59
	v_add_f32_e32 v2, v5, v2
	v_max_f32_e32 v16, 0, v2
	ds_read_b128 v[2:5], v22 offset:53600
	s_waitcnt lgkmcnt(0)
	v_add_f32_e32 v2, v17, v2
	v_max_f32_e32 v17, 0, v2
	v_accvgpr_read_b32 v2, a61
	v_add_f32_e32 v2, v3, v2
	v_max_f32_e32 v18, 0, v2
	v_accvgpr_read_b32 v2, a62
	v_add_f32_e32 v2, v4, v2
	v_max_f32_e32 v19, 0, v2
	v_accvgpr_read_b32 v2, a63
	v_add_f32_e32 v2, v5, v2
	v_max_f32_e32 v20, 0, v2
	v_cvt_pk_f16_f32 v4, v9, v10
	v_cvt_pk_f16_f32 v3, v7, v8
	v_cvt_pk_f16_f32 v2, v1, v6
	ds_read_b128 v[6:9], v0 offset:45056
	v_cvt_pk_f16_f32 v5, v11, v12
	v_accvgpr_read_b32 v1, a32
	s_waitcnt lgkmcnt(0)
	v_mfma_f32_32x32x16_f16 a[80:95], v[6:9], v[2:5], a[80:95]
	ds_read_b128 v[6:9], v0 offset:46080
	v_cvt_pk_f16_f32 v5, v19, v20
	v_cvt_pk_f16_f32 v4, v17, v18
	v_cvt_pk_f16_f32 v3, v15, v16
	v_cvt_pk_f16_f32 v2, v13, v14
	v_accvgpr_read_b32 v13, a40
	v_accvgpr_read_b32 v17, a44
	s_waitcnt lgkmcnt(0)
	v_mfma_f32_32x32x16_f16 a[80:95], v[6:9], v[2:5], a[80:95]
	ds_read_b128 v[2:5], v22 offset:53632
	v_accvgpr_read_b32 v9, a36
	s_waitcnt lgkmcnt(0)
	v_add_f32_e32 v1, v1, v2
	v_accvgpr_read_b32 v2, a33
	v_add_f32_e32 v2, v3, v2
	v_max_f32_e32 v6, 0, v2
	v_accvgpr_read_b32 v2, a34
	v_add_f32_e32 v2, v4, v2
	v_max_f32_e32 v7, 0, v2
	v_accvgpr_read_b32 v2, a35
	v_add_f32_e32 v2, v5, v2
	v_max_f32_e32 v8, 0, v2
	ds_read_b128 v[2:5], v22 offset:53664
	v_max_f32_e32 v1, 0, v1
	s_waitcnt lgkmcnt(0)
	v_add_f32_e32 v2, v9, v2
	v_max_f32_e32 v9, 0, v2
	v_accvgpr_read_b32 v2, a37
	v_add_f32_e32 v2, v3, v2
	v_max_f32_e32 v10, 0, v2
	v_accvgpr_read_b32 v2, a38
	v_add_f32_e32 v2, v4, v2
	v_max_f32_e32 v11, 0, v2
	v_accvgpr_read_b32 v2, a39
	v_add_f32_e32 v2, v5, v2
	v_max_f32_e32 v12, 0, v2
	ds_read_b128 v[2:5], v22 offset:53696
	s_waitcnt lgkmcnt(0)
	v_add_f32_e32 v2, v13, v2
	v_max_f32_e32 v13, 0, v2
	v_accvgpr_read_b32 v2, a41
	v_add_f32_e32 v2, v3, v2
	v_max_f32_e32 v14, 0, v2
	v_accvgpr_read_b32 v2, a42
	v_add_f32_e32 v2, v4, v2
	v_max_f32_e32 v15, 0, v2
	v_accvgpr_read_b32 v2, a43
	v_add_f32_e32 v2, v5, v2
	v_max_f32_e32 v16, 0, v2
	ds_read_b128 v[2:5], v22 offset:53728
	s_waitcnt lgkmcnt(0)
	v_add_f32_e32 v2, v17, v2
	v_max_f32_e32 v17, 0, v2
	v_accvgpr_read_b32 v2, a45
	v_add_f32_e32 v2, v3, v2
	v_max_f32_e32 v18, 0, v2
	v_accvgpr_read_b32 v2, a46
	v_add_f32_e32 v2, v4, v2
	v_max_f32_e32 v19, 0, v2
	v_accvgpr_read_b32 v2, a47
	v_add_f32_e32 v2, v5, v2
	v_max_f32_e32 v20, 0, v2
	v_cvt_pk_f16_f32 v4, v9, v10
	v_cvt_pk_f16_f32 v3, v7, v8
	v_cvt_pk_f16_f32 v2, v1, v6
	ds_read_b128 v[6:9], v0 offset:47104
	v_cvt_pk_f16_f32 v5, v11, v12
	v_accvgpr_read_b32 v1, a16
	s_waitcnt lgkmcnt(0)
	v_mfma_f32_32x32x16_f16 a[32:47], v[6:9], v[2:5], 0
	ds_read_b128 v[6:9], v0 offset:48128
	v_cvt_pk_f16_f32 v5, v19, v20
	v_cvt_pk_f16_f32 v4, v17, v18
	v_cvt_pk_f16_f32 v3, v15, v16
	v_cvt_pk_f16_f32 v2, v13, v14
	v_accvgpr_read_b32 v13, a24
	v_accvgpr_read_b32 v17, a28
	s_waitcnt lgkmcnt(0)
	v_mfma_f32_32x32x16_f16 a[32:47], v[6:9], v[2:5], a[32:47]
	ds_read_b128 v[2:5], v22 offset:53760
	v_accvgpr_read_b32 v9, a20
	s_waitcnt lgkmcnt(0)
	v_add_f32_e32 v1, v1, v2
	v_accvgpr_read_b32 v2, a17
	v_add_f32_e32 v2, v3, v2
	v_max_f32_e32 v6, 0, v2
	v_accvgpr_read_b32 v2, a18
	v_add_f32_e32 v2, v4, v2
	v_max_f32_e32 v7, 0, v2
	v_accvgpr_read_b32 v2, a19
	v_add_f32_e32 v2, v5, v2
	v_max_f32_e32 v8, 0, v2
	ds_read_b128 v[2:5], v22 offset:53792
	v_max_f32_e32 v1, 0, v1
	s_waitcnt lgkmcnt(0)
	v_add_f32_e32 v2, v9, v2
	v_max_f32_e32 v9, 0, v2
	v_accvgpr_read_b32 v2, a21
	v_add_f32_e32 v2, v3, v2
	v_max_f32_e32 v10, 0, v2
	v_accvgpr_read_b32 v2, a22
	v_add_f32_e32 v2, v4, v2
	v_max_f32_e32 v11, 0, v2
	v_accvgpr_read_b32 v2, a23
	v_add_f32_e32 v2, v5, v2
	v_max_f32_e32 v12, 0, v2
	ds_read_b128 v[2:5], v22 offset:53824
	s_waitcnt lgkmcnt(0)
	v_add_f32_e32 v2, v13, v2
	v_max_f32_e32 v13, 0, v2
	v_accvgpr_read_b32 v2, a25
	v_add_f32_e32 v2, v3, v2
	v_max_f32_e32 v14, 0, v2
	v_accvgpr_read_b32 v2, a26
	v_add_f32_e32 v2, v4, v2
	v_max_f32_e32 v15, 0, v2
	v_accvgpr_read_b32 v2, a27
	v_add_f32_e32 v2, v5, v2
	v_max_f32_e32 v16, 0, v2
	ds_read_b128 v[2:5], v22 offset:53856
	s_waitcnt lgkmcnt(0)
	v_add_f32_e32 v2, v17, v2
	v_max_f32_e32 v17, 0, v2
	v_accvgpr_read_b32 v2, a29
	v_add_f32_e32 v2, v3, v2
	v_max_f32_e32 v18, 0, v2
	v_accvgpr_read_b32 v2, a30
	v_add_f32_e32 v2, v4, v2
	v_max_f32_e32 v19, 0, v2
	v_accvgpr_read_b32 v2, a31
	v_add_f32_e32 v2, v5, v2
	v_max_f32_e32 v20, 0, v2
	v_cvt_pk_f16_f32 v4, v9, v10
	v_cvt_pk_f16_f32 v3, v7, v8
	v_cvt_pk_f16_f32 v2, v1, v6
	ds_read_b128 v[6:9], v0 offset:49152
	v_cvt_pk_f16_f32 v5, v11, v12
	v_accvgpr_read_b32 v1, a0
	s_waitcnt lgkmcnt(0)
	v_mfma_f32_32x32x16_f16 a[32:47], v[6:9], v[2:5], a[32:47]
	ds_read_b128 v[6:9], v0 offset:50176
	v_cvt_pk_f16_f32 v5, v19, v20
	v_cvt_pk_f16_f32 v4, v17, v18
	v_cvt_pk_f16_f32 v3, v15, v16
	v_cvt_pk_f16_f32 v2, v13, v14
	v_accvgpr_read_b32 v13, a8
	v_accvgpr_read_b32 v17, a12
	s_waitcnt lgkmcnt(0)
	v_mfma_f32_32x32x16_f16 a[32:47], v[6:9], v[2:5], a[32:47]
	ds_read_b128 v[2:5], v22 offset:53888
	v_accvgpr_read_b32 v9, a4
	s_waitcnt lgkmcnt(0)
	v_add_f32_e32 v1, v1, v2
	v_accvgpr_read_b32 v2, a1
	v_add_f32_e32 v2, v3, v2
	v_max_f32_e32 v6, 0, v2
	v_accvgpr_read_b32 v2, a2
	v_add_f32_e32 v2, v4, v2
	v_max_f32_e32 v7, 0, v2
	v_accvgpr_read_b32 v2, a3
	v_add_f32_e32 v2, v5, v2
	v_max_f32_e32 v8, 0, v2
	ds_read_b128 v[2:5], v22 offset:53920
	v_max_f32_e32 v1, 0, v1
	s_waitcnt lgkmcnt(0)
	v_add_f32_e32 v2, v9, v2
	v_max_f32_e32 v9, 0, v2
	v_accvgpr_read_b32 v2, a5
	v_add_f32_e32 v2, v3, v2
	v_max_f32_e32 v10, 0, v2
	v_accvgpr_read_b32 v2, a6
	v_add_f32_e32 v2, v4, v2
	v_max_f32_e32 v11, 0, v2
	v_accvgpr_read_b32 v2, a7
	v_add_f32_e32 v2, v5, v2
	v_max_f32_e32 v12, 0, v2
	ds_read_b128 v[2:5], v22 offset:53952
	s_waitcnt lgkmcnt(0)
	v_add_f32_e32 v2, v13, v2
	v_max_f32_e32 v13, 0, v2
	v_accvgpr_read_b32 v2, a9
	v_add_f32_e32 v2, v3, v2
	v_max_f32_e32 v14, 0, v2
	v_accvgpr_read_b32 v2, a10
	v_add_f32_e32 v2, v4, v2
	v_max_f32_e32 v15, 0, v2
	v_accvgpr_read_b32 v2, a11
	v_add_f32_e32 v2, v5, v2
	v_max_f32_e32 v16, 0, v2
	ds_read_b128 v[2:5], v22 offset:53984
	s_waitcnt lgkmcnt(0)
	v_add_f32_e32 v2, v17, v2
	v_max_f32_e32 v17, 0, v2
	v_accvgpr_read_b32 v2, a13
	v_add_f32_e32 v2, v3, v2
	v_max_f32_e32 v18, 0, v2
	v_accvgpr_read_b32 v2, a14
	v_add_f32_e32 v2, v4, v2
	v_max_f32_e32 v19, 0, v2
	v_accvgpr_read_b32 v2, a15
	v_add_f32_e32 v2, v5, v2
	v_max_f32_e32 v20, 0, v2
	v_cvt_pk_f16_f32 v4, v9, v10
	v_cvt_pk_f16_f32 v3, v7, v8
	v_cvt_pk_f16_f32 v2, v1, v6
	ds_read_b128 v[6:9], v0 offset:51200
	v_cvt_pk_f16_f32 v5, v11, v12
	s_waitcnt lgkmcnt(0)
	s_nop 0
	v_mfma_f32_32x32x16_f16 a[32:47], v[6:9], v[2:5], a[32:47]
	ds_read_b128 v[6:9], v0 offset:52224
	v_cvt_pk_f16_f32 v5, v19, v20
	v_cvt_pk_f16_f32 v4, v17, v18
	v_cvt_pk_f16_f32 v3, v15, v16
	v_cvt_pk_f16_f32 v2, v13, v14
	s_waitcnt lgkmcnt(0)
	s_nop 0
	v_mfma_f32_32x32x16_f16 a[32:47], v[6:9], v[2:5], a[32:47]
	s_and_saveexec_b64 s[2:3], s[0:1]
	s_cbranch_execz .LBB3_39
	v_accvgpr_read_b32 v0, a80
	v_accvgpr_read_b32 v6, a86
	v_accvgpr_read_b32 v7, a87
	v_accvgpr_read_b32 v8, a88
	v_accvgpr_read_b32 v9, a89
	v_accvgpr_read_b32 v10, a90
	v_accvgpr_read_b32 v11, a91
	v_accvgpr_read_b32 v12, a92
	v_accvgpr_read_b32 v13, a93
	v_accvgpr_read_b32 v14, a94
	v_accvgpr_read_b32 v15, a95
	v_accvgpr_read_b32 v6, a32
	v_accvgpr_read_b32 v14, a40
	v_accvgpr_read_b32 v15, a41
	v_accvgpr_read_b32 v16, a42
	v_accvgpr_read_b32 v17, a43
	v_accvgpr_read_b32 v18, a44
	v_accvgpr_read_b32 v19, a45
	v_accvgpr_read_b32 v20, a46
	v_accvgpr_read_b32 v21, a47
	ds_read_b128 v[14:17], v22 offset:54016
	ds_read_b128 v[18:21], v22 offset:54080
	v_accvgpr_read_b32 v12, a38
	v_accvgpr_read_b32 v13, a39
	v_lshlrev_b32_e32 v24, 2, v85
	v_accvgpr_read_b32 v1, a81
	v_accvgpr_read_b32 v7, a33
	v_mad_i64_i32 v[12:13], s[0:1], v80, 40, s[18:19]
	v_ashrrev_i32_e32 v25, 31, v24
	v_accvgpr_read_b32 v3, a83
	v_accvgpr_read_b32 v9, a35
	v_lshl_add_u64 v[22:23], v[24:25], 2, v[12:13]
	v_mov_b32_e32 v25, v1
	s_waitcnt lgkmcnt(1)
	v_mov_b32_e32 v27, v15
	v_mov_b32_e32 v1, v7
	s_waitcnt lgkmcnt(0)
	v_mov_b32_e32 v15, v19
	v_accvgpr_read_b32 v2, a82
	v_accvgpr_read_b32 v8, a34
	v_pk_add_f32 v[0:1], v[0:1], v[14:15]
	v_mov_b32_e32 v7, v3
	v_mov_b32_e32 v15, v17
	v_mov_b32_e32 v3, v9
	v_mov_b32_e32 v17, v21
	v_mov_b32_e32 v24, v6
	v_mov_b32_e32 v26, v18
	v_mov_b32_e32 v6, v8
	v_mov_b32_e32 v14, v20
	v_pk_add_f32 v[2:3], v[2:3], v[16:17]
	v_pk_add_f32 v[24:25], v[24:25], v[26:27]
	s_waitcnt vmcnt(0)
	v_pk_mul_f32 v[0:1], v[82:83], v[0:1]
	v_pk_add_f32 v[6:7], v[6:7], v[14:15]
	v_pk_mul_f32 v[2:3], v[82:83], v[2:3]
	v_accvgpr_read_b32 v4, a84
	v_accvgpr_read_b32 v5, a85
	v_accvgpr_read_b32 v10, a36
	v_accvgpr_read_b32 v11, a37
	v_pk_fma_f32 v[0:1], v[82:83], v[24:25], v[0:1] op_sel:[1,0,0] op_sel_hi:[0,1,1]
	v_pk_fma_f32 v[2:3], v[82:83], v[6:7], v[2:3] op_sel:[1,0,0] op_sel_hi:[0,1,1]
	v_cmp_eq_u32_e32 vcc, 0, v85
	global_store_dwordx4 v[22:23], v[0:3], off
	s_and_b64 exec, exec, vcc
	s_cbranch_execz .LBB3_39
	s_mov_b32 s0, 0xd000
	v_add_u32_e64 v0, s0, 0
	ds_read2_b64 v[0:3], v0 offset0:100 offset1:108
	v_mov_b32_e32 v9, v5
	v_mov_b32_e32 v5, v11
	v_mov_b32_e32 v8, v10
	v_pk_mov_b32 v[6:7], v[82:83], v[82:83] op_sel:[1,0]
	s_waitcnt lgkmcnt(0)
	v_mov_b32_e32 v15, v1
	v_mov_b32_e32 v1, v3
	v_mov_b32_e32 v14, v2
	v_pk_add_f32 v[0:1], v[4:5], v[0:1]
	v_pk_add_f32 v[8:9], v[8:9], v[14:15]
	v_pk_mul_f32 v[0:1], v[82:83], v[0:1]
	s_nop 0
	v_pk_fma_f32 v[0:1], v[6:7], v[8:9], v[0:1]
	global_store_dwordx2 v[12:13], v[0:1], off offset:32
